# v27: v26 with rotating table-load issue (block b+4's loads issued as soon as block b is consumed)
# baseline (speedup 1.0000x reference)
.LBB0_157:
	v_mul_f32_e32 v192, v189, v189
	v_mul_f32_e32 v193, v181, v181
	v_fmac_f32_e32 v192, v188, v188
	v_fmac_f32_e32 v193, v180, v180
	v_fmac_f32_e32 v192, v190, v190
	v_fmac_f32_e32 v193, v182, v182
	v_fmac_f32_e32 v192, v191, v191
	v_fmac_f32_e32 v193, v183, v183
	v_mov_b32_e32 v194, v165
	v_mov_b32_e32 v195, v173
	v_add_f32_e32 v196, v193, v192
	v_mov_b32_e32 v192, v164
	v_mov_b32_e32 v193, v172
	v_pk_mul_f32 v[194:195], v[194:195], v[194:195]
	s_nop 0
	v_pk_fma_f32 v[192:193], v[192:193], v[192:193], v[194:195]
	v_mov_b32_e32 v194, v166
	v_mov_b32_e32 v195, v174
	v_pk_fma_f32 v[192:193], v[194:195], v[194:195], v[192:193]
	v_mov_b32_e32 v194, v167
	v_mov_b32_e32 v195, v175
	v_pk_fma_f32 v[192:193], v[194:195], v[194:195], v[192:193]
	v_mov_b32_e32 v194, v149
	v_add_f32_e32 v193, v193, v196
	v_mov_b32_e32 v195, v157
	v_add_f32_e32 v196, v192, v193
	v_mov_b32_e32 v192, v148
	v_mov_b32_e32 v193, v156
	v_pk_mul_f32 v[194:195], v[194:195], v[194:195]
	s_nop 0
	v_pk_fma_f32 v[192:193], v[192:193], v[192:193], v[194:195]
	v_mov_b32_e32 v194, v150
	v_mov_b32_e32 v195, v158
	v_pk_fma_f32 v[192:193], v[194:195], v[194:195], v[192:193]
	v_mov_b32_e32 v194, v151
	v_mov_b32_e32 v195, v159
	v_pk_fma_f32 v[192:193], v[194:195], v[194:195], v[192:193]
	v_mov_b32_e32 v194, v133
	v_add_f32_e32 v193, v193, v196
	v_mov_b32_e32 v195, v141
	v_add_f32_e32 v196, v192, v193
	v_mov_b32_e32 v192, v132
	v_mov_b32_e32 v193, v140
	v_pk_mul_f32 v[194:195], v[194:195], v[194:195]
	s_nop 0
	v_pk_fma_f32 v[192:193], v[192:193], v[192:193], v[194:195]
	v_mov_b32_e32 v194, v134
	v_mov_b32_e32 v195, v142
	v_pk_fma_f32 v[192:193], v[194:195], v[194:195], v[192:193]
	v_mov_b32_e32 v194, v135
	v_mov_b32_e32 v195, v143
	v_pk_fma_f32 v[192:193], v[194:195], v[194:195], v[192:193]
	s_nop 0
	v_add_f32_e32 v193, v193, v196
	v_add_f32_e32 v192, v192, v193
	s_nop 1
	v_add_f32_dpp v192, v192, v192 quad_perm:[1,0,3,2] row_mask:0xf bank_mask:0xf bound_ctrl:1
	s_nop 1
	v_add_f32_dpp v192, v192, v192 quad_perm:[2,3,0,1] row_mask:0xf bank_mask:0xf bound_ctrl:1
	s_nop 1
	v_add_f32_dpp v192, v192, v192 row_half_mirror row_mask:0xf bank_mask:0xf bound_ctrl:1
	s_nop 1
	v_add_f32_dpp v192, v192, v192 row_mirror row_mask:0xf bank_mask:0xf bound_ctrl:1
	s_nop 0
	v_readlane_b32 s13, v192, 16
	v_readlane_b32 s16, v192, 48
	v_readlane_b32 s4, v192, 0
	v_readlane_b32 s5, v192, 32
	v_mov_b32_e32 v192, s13
	v_mov_b32_e32 v193, s16
	v_pk_add_f32 v[192:193], s[4:5], v[192:193]
	s_nop 0
	v_add_f32_e32 v192, v192, v193
	v_fmamk_f32 v192, v192, 0x3a000000, v241
	v_cmp_gt_f32_e32 vcc, s34, v192
	v_mul_f32_e32 v193, 0x4f800000, v192
	s_nop 0
	v_cndmask_b32_e32 v192, v192, v193, vcc
	v_sqrt_f32_e32 v193, v192
	s_nop 0
	v_add_u32_e32 v194, -1, v193
	v_fma_f32 v195, -v194, v193, v192
	v_cmp_ge_f32_e64 s[4:5], 0, v195
	v_add_u32_e32 v195, 1, v193
	s_nop 0
	v_cndmask_b32_e64 v194, v193, v194, s[4:5]
	v_fma_f32 v193, -v195, v193, v192
	v_cmp_lt_f32_e64 s[4:5], 0, v193
	s_nop 1
	v_cndmask_b32_e64 v193, v194, v195, s[4:5]
	v_mul_f32_e32 v194, 0x37800000, v193
	v_cndmask_b32_e32 v193, v193, v194, vcc
	v_cmp_class_f32_e32 vcc, v192, v242
	s_nop 1
	v_cndmask_b32_e32 v192, v193, v192, vcc
	v_div_scale_f32 v193, s[4:5], v192, v192, 1.0
	v_rcp_f32_e32 v194, v193
	s_nop 0
	v_fma_f32 v195, -v193, v194, 1.0
	v_fmac_f32_e32 v194, v195, v194
	v_div_scale_f32 v195, vcc, 1.0, v192, 1.0
	v_mul_f32_e32 v196, v195, v194
	v_fma_f32 v197, -v193, v196, v195
	v_fmac_f32_e32 v196, v197, v194
	v_fma_f32 v193, -v193, v196, v195
	v_div_fmas_f32 v193, v193, v194, v196
	v_div_fixup_f32 v204, v193, v192, 1.0
	v_mul_f32_e32 v192, v185, v185
	v_mul_f32_e32 v193, v177, v177
	v_fmac_f32_e32 v192, v184, v184
	v_fmac_f32_e32 v193, v176, v176
	v_fmac_f32_e32 v192, v186, v186
	v_fmac_f32_e32 v193, v178, v178
	v_fmac_f32_e32 v192, v187, v187
	v_fmac_f32_e32 v193, v179, v179
	v_mov_b32_e32 v194, v161
	v_mov_b32_e32 v195, v169
	v_add_f32_e32 v196, v193, v192
	v_mov_b32_e32 v192, v160
	v_mov_b32_e32 v193, v168
	v_pk_mul_f32 v[194:195], v[194:195], v[194:195]
	s_nop 0
	v_pk_fma_f32 v[192:193], v[192:193], v[192:193], v[194:195]
	v_mov_b32_e32 v194, v162
	v_mov_b32_e32 v195, v170
	v_pk_fma_f32 v[192:193], v[194:195], v[194:195], v[192:193]
	v_mov_b32_e32 v194, v163
	v_mov_b32_e32 v195, v171
	v_pk_fma_f32 v[192:193], v[194:195], v[194:195], v[192:193]
	v_mov_b32_e32 v194, v145
	v_add_f32_e32 v193, v193, v196
	v_mov_b32_e32 v195, v153
	v_add_f32_e32 v196, v192, v193
	v_mov_b32_e32 v192, v144
	v_mov_b32_e32 v193, v152
	v_pk_mul_f32 v[194:195], v[194:195], v[194:195]
	s_nop 0
	v_pk_fma_f32 v[192:193], v[192:193], v[192:193], v[194:195]
	v_mov_b32_e32 v194, v146
	v_mov_b32_e32 v195, v154
	v_pk_fma_f32 v[192:193], v[194:195], v[194:195], v[192:193]
	v_mov_b32_e32 v194, v147
	v_mov_b32_e32 v195, v155
	v_pk_fma_f32 v[192:193], v[194:195], v[194:195], v[192:193]
	v_mov_b32_e32 v194, v129
	v_add_f32_e32 v193, v193, v196
	v_mov_b32_e32 v195, v137
	v_add_f32_e32 v196, v192, v193
	v_mov_b32_e32 v192, v128
	v_mov_b32_e32 v193, v136
	v_pk_mul_f32 v[194:195], v[194:195], v[194:195]
	s_nop 0
	v_pk_fma_f32 v[192:193], v[192:193], v[192:193], v[194:195]
	v_mov_b32_e32 v194, v130
	v_mov_b32_e32 v195, v138
	v_pk_fma_f32 v[192:193], v[194:195], v[194:195], v[192:193]
	v_mov_b32_e32 v194, v131
	v_mov_b32_e32 v195, v139
	v_pk_fma_f32 v[192:193], v[194:195], v[194:195], v[192:193]
	s_nop 0
	v_add_f32_e32 v193, v193, v196
	v_add_f32_e32 v192, v192, v193
	s_nop 1
	v_add_f32_dpp v192, v192, v192 quad_perm:[1,0,3,2] row_mask:0xf bank_mask:0xf bound_ctrl:1
	s_nop 1
	v_add_f32_dpp v192, v192, v192 quad_perm:[2,3,0,1] row_mask:0xf bank_mask:0xf bound_ctrl:1
	s_nop 1
	v_add_f32_dpp v192, v192, v192 row_half_mirror row_mask:0xf bank_mask:0xf bound_ctrl:1
	s_nop 1
	v_add_f32_dpp v192, v192, v192 row_mirror row_mask:0xf bank_mask:0xf bound_ctrl:1
	s_nop 0
	v_readlane_b32 s13, v192, 16
	v_readlane_b32 s16, v192, 48
	v_readlane_b32 s4, v192, 0
	v_readlane_b32 s5, v192, 32
	v_mov_b32_e32 v192, s13
	v_mov_b32_e32 v193, s16
	v_pk_add_f32 v[192:193], s[4:5], v[192:193]
	s_nop 0
	v_add_f32_e32 v192, v192, v193
	v_fmamk_f32 v192, v192, 0x3a000000, v241
	v_cmp_gt_f32_e32 vcc, s34, v192
	v_mul_f32_e32 v193, 0x4f800000, v192
	s_nop 0
	v_cndmask_b32_e32 v192, v192, v193, vcc
	v_sqrt_f32_e32 v193, v192
	s_nop 0
	v_add_u32_e32 v194, -1, v193
	v_fma_f32 v195, -v194, v193, v192
	v_cmp_ge_f32_e64 s[4:5], 0, v195
	v_add_u32_e32 v195, 1, v193
	s_nop 0
	v_cndmask_b32_e64 v194, v193, v194, s[4:5]
	v_fma_f32 v193, -v195, v193, v192
	v_cmp_lt_f32_e64 s[4:5], 0, v193
	s_nop 1
	v_cndmask_b32_e64 v193, v194, v195, s[4:5]
	v_mul_f32_e32 v194, 0x37800000, v193
	v_cndmask_b32_e32 v193, v193, v194, vcc
	v_cmp_class_f32_e32 vcc, v192, v242
	s_nop 1
	v_cndmask_b32_e32 v192, v193, v192, vcc
	v_div_scale_f32 v193, s[4:5], v192, v192, 1.0
	v_rcp_f32_e32 v194, v193
	s_ashr_i32 s4, s12, 12
	s_mul_hi_i32 s5, s4, 0xc000
	s_mul_i32 s4, s4, 0xc000
	v_fma_f32 v195, -v193, v194, 1.0
	v_fmac_f32_e32 v194, v195, v194
	v_div_scale_f32 v195, vcc, 1.0, v192, 1.0
	v_mul_f32_e32 v196, v195, v194
	v_fma_f32 v197, -v193, v196, v195
	s_add_u32 s16, s25, s4
	v_fmac_f32_e32 v196, v197, v194
	s_addc_u32 s17, s26, s5
	s_ashr_i32 s13, s12, 31
	v_fma_f32 v193, -v193, v196, v195
	s_lshl_b64 s[4:5], s[12:13], 12
	v_div_fmas_f32 v193, v193, v194, v196
	s_add_u32 s4, s1, s4
	v_div_fixup_f32 v224, v193, v192, 1.0
	s_addc_u32 s5, s20, s5
	v_lshlrev_b64 v[192:193], 1, v[222:223]
	v_lshl_add_u64 v[194:195], s[4:5], 0, v[192:193]
	v_cvt_pk_bf16_f32 v196, v188, v189
	v_cvt_pk_bf16_f32 v197, v190, v191
	global_store_dwordx2 v[194:195], v[196:197], off
	v_lshlrev_b64 v[194:195], 1, v[220:221]
	v_lshl_add_u64 v[196:197], s[4:5], 0, v[194:195]
	v_cvt_pk_bf16_f32 v198, v180, v181
	v_cvt_pk_bf16_f32 v199, v182, v183
	global_store_dwordx2 v[196:197], v[198:199], off
	v_lshlrev_b64 v[196:197], 1, v[218:219]
	v_lshl_add_u64 v[198:199], s[4:5], 0, v[196:197]
	v_cvt_pk_bf16_f32 v200, v172, v173
	v_cvt_pk_bf16_f32 v201, v174, v175
	global_store_dwordx2 v[198:199], v[200:201], off
	v_lshlrev_b64 v[198:199], 1, v[216:217]
	v_lshl_add_u64 v[200:201], s[4:5], 0, v[198:199]
	v_cvt_pk_bf16_f32 v202, v164, v165
	v_cvt_pk_bf16_f32 v203, v166, v167
	global_store_dwordx2 v[200:201], v[202:203], off
	v_lshlrev_b64 v[200:201], 1, v[214:215]
	v_lshl_add_u64 v[202:203], s[4:5], 0, v[200:201]
	v_cvt_pk_bf16_f32 v248, v156, v157
	v_cvt_pk_bf16_f32 v249, v158, v159
	global_store_dwordx2 v[202:203], v[248:249], off
	v_lshlrev_b64 v[202:203], 1, v[212:213]
	v_lshl_add_u64 v[248:249], s[4:5], 0, v[202:203]
	v_cvt_pk_bf16_f32 v250, v148, v149
	v_cvt_pk_bf16_f32 v251, v150, v151
	global_store_dwordx2 v[248:249], v[250:251], off
	v_lshlrev_b64 v[248:249], 1, v[210:211]
	v_lshl_add_u64 v[250:251], s[4:5], 0, v[248:249]
	v_cvt_pk_bf16_f32 v244, v140, v141
	v_cvt_pk_bf16_f32 v245, v142, v143
	global_store_dwordx2 v[250:251], v[244:245], off
	v_lshlrev_b64 v[244:245], 1, v[208:209]
	v_lshl_add_u64 v[250:251], s[4:5], 0, v[244:245]
	s_add_i32 s4, s21, s12
	s_ashr_i32 s5, s4, 31
	s_lshl_b64 s[18:19], s[4:5], 12
	s_add_u32 s18, s1, s18
	s_addc_u32 s19, s20, s19
	v_cvt_pk_bf16_f32 v246, v132, v133
	v_cvt_pk_bf16_f32 v247, v134, v135
	v_lshl_add_u64 v[192:193], s[18:19], 0, v[192:193]
	global_store_dwordx2 v[250:251], v[246:247], off
	v_cvt_pk_bf16_f32 v246, v184, v185
	v_cvt_pk_bf16_f32 v247, v186, v187
	global_store_dwordx2 v[192:193], v[246:247], off
	v_lshl_add_u64 v[192:193], s[18:19], 0, v[194:195]
	v_cvt_pk_bf16_f32 v194, v176, v177
	v_cvt_pk_bf16_f32 v195, v178, v179
	global_store_dwordx2 v[192:193], v[194:195], off
	v_lshl_add_u64 v[192:193], s[18:19], 0, v[196:197]
	v_cvt_pk_bf16_f32 v194, v168, v169
	v_cvt_pk_bf16_f32 v195, v170, v171
	global_store_dwordx2 v[192:193], v[194:195], off
	v_lshl_add_u64 v[192:193], s[18:19], 0, v[198:199]
	v_cvt_pk_bf16_f32 v194, v160, v161
	v_cvt_pk_bf16_f32 v195, v162, v163
	global_store_dwordx2 v[192:193], v[194:195], off
	v_lshl_add_u64 v[192:193], s[18:19], 0, v[200:201]
	v_cvt_pk_bf16_f32 v194, v152, v153
	v_cvt_pk_bf16_f32 v195, v154, v155
	global_store_dwordx2 v[192:193], v[194:195], off
	v_lshl_add_u64 v[192:193], s[18:19], 0, v[202:203]
	v_cvt_pk_bf16_f32 v194, v144, v145
	v_cvt_pk_bf16_f32 v195, v146, v147
	global_store_dwordx2 v[192:193], v[194:195], off
	v_lshl_add_u64 v[192:193], s[18:19], 0, v[248:249]
	v_cvt_pk_bf16_f32 v194, v136, v137
	v_cvt_pk_bf16_f32 v195, v138, v139
	global_store_dwordx2 v[192:193], v[194:195], off
	v_lshl_add_u64 v[192:193], s[18:19], 0, v[244:245]
	s_add_u32 s18, s16, 0x2000
	v_cvt_pk_bf16_f32 v194, v128, v129
	v_cvt_pk_bf16_f32 v195, v130, v131
	global_store_dwordx2 v[192:193], v[194:195], off
	s_addc_u32 s19, s17, 0
	v_lshlrev_b32_e32 v192, 3, v226
	v_lshlrev_b64 v[196:197], 2, v[222:223]
	v_and_b32_e32 v207, 8, v192
	v_lshl_add_u64 v[192:193], s[8:9], 0, v[196:197]
	v_lshl_add_u64 v[198:199], s[18:19], 0, v[196:197]
	v_lshlrev_b32_e32 v112, 4, v226
	v_add_u32_e32 v113, 0x1000, v112
	global_load_dwordx4 v[64:67], v112, s[8:9]
	global_load_dwordx4 v[68:71], v112, s[18:19]
	global_load_dwordx4 v[72:75], v112, s[16:17]
	global_load_dwordx4 v[76:79], v112, s[8:9] offset:1024
	global_load_dwordx4 v[80:83], v112, s[18:19] offset:1024
	global_load_dwordx4 v[84:87], v112, s[16:17] offset:1024
	global_load_dwordx4 v[88:91], v112, s[8:9] offset:2048
	global_load_dwordx4 v[92:95], v112, s[18:19] offset:2048
	global_load_dwordx4 v[96:99], v112, s[16:17] offset:2048
	global_load_dwordx4 v[100:103], v112, s[8:9] offset:3072
	global_load_dwordx4 v[104:107], v112, s[18:19] offset:3072
	global_load_dwordx4 v[108:111], v112, s[16:17] offset:3072
	v_lshl_add_u64 v[196:197], s[16:17], 0, v[196:197]
	v_pk_mul_f32 v[188:189], v[188:189], v[204:205] op_sel_hi:[1,0]
	v_pk_mul_f32 v[190:191], v[190:191], v[204:205] op_sel_hi:[1,0]
	v_lshrrev_b32_e32 v248, 1, v226
	v_pk_mul_f32 v[184:185], v[184:185], v[224:225] op_sel_hi:[1,0]
	v_pk_mul_f32 v[186:187], v[186:187], v[224:225] op_sel_hi:[1,0]
	v_pk_mul_f32 v[180:181], v[180:181], v[204:205] op_sel_hi:[1,0]
	v_pk_mul_f32 v[182:183], v[182:183], v[204:205] op_sel_hi:[1,0]
	v_pk_mul_f32 v[176:177], v[176:177], v[224:225] op_sel_hi:[1,0]
	v_pk_mul_f32 v[178:179], v[178:179], v[224:225] op_sel_hi:[1,0]
	v_pk_mul_f32 v[172:173], v[172:173], v[204:205] op_sel_hi:[1,0]
	v_pk_mul_f32 v[174:175], v[174:175], v[204:205] op_sel_hi:[1,0]
	v_pk_mul_f32 v[168:169], v[168:169], v[224:225] op_sel_hi:[1,0]
	v_pk_mul_f32 v[170:171], v[170:171], v[224:225] op_sel_hi:[1,0]
	v_pk_mul_f32 v[164:165], v[164:165], v[204:205] op_sel_hi:[1,0]
	v_pk_mul_f32 v[166:167], v[166:167], v[204:205] op_sel_hi:[1,0]
	v_pk_mul_f32 v[160:161], v[160:161], v[224:225] op_sel_hi:[1,0]
	v_pk_mul_f32 v[162:163], v[162:163], v[224:225] op_sel_hi:[1,0]
	v_pk_mul_f32 v[156:157], v[156:157], v[204:205] op_sel_hi:[1,0]
	v_pk_mul_f32 v[158:159], v[158:159], v[204:205] op_sel_hi:[1,0]
	v_pk_mul_f32 v[152:153], v[152:153], v[224:225] op_sel_hi:[1,0]
	v_pk_mul_f32 v[154:155], v[154:155], v[224:225] op_sel_hi:[1,0]
	v_pk_mul_f32 v[148:149], v[148:149], v[204:205] op_sel_hi:[1,0]
	v_pk_mul_f32 v[150:151], v[150:151], v[204:205] op_sel_hi:[1,0]
	v_pk_mul_f32 v[144:145], v[144:145], v[224:225] op_sel_hi:[1,0]
	v_pk_mul_f32 v[146:147], v[146:147], v[224:225] op_sel_hi:[1,0]
	v_pk_mul_f32 v[140:141], v[140:141], v[204:205] op_sel_hi:[1,0]
	v_pk_mul_f32 v[142:143], v[142:143], v[204:205] op_sel_hi:[1,0]
	v_pk_mul_f32 v[136:137], v[136:137], v[224:225] op_sel_hi:[1,0]
	v_pk_mul_f32 v[138:139], v[138:139], v[224:225] op_sel_hi:[1,0]
	v_pk_mul_f32 v[132:133], v[132:133], v[204:205] op_sel_hi:[1,0]
	v_pk_mul_f32 v[134:135], v[134:135], v[204:205] op_sel_hi:[1,0]
	v_pk_mul_f32 v[128:129], v[128:129], v[224:225] op_sel_hi:[1,0]
	v_pk_mul_f32 v[130:131], v[130:131], v[224:225] op_sel_hi:[1,0]
	s_waitcnt vmcnt(11)
	v_pk_mul_f32 v[244:245], v[188:189], v[64:65]
	v_pk_mul_f32 v[188:189], v[190:191], v[66:67]
	s_waitcnt vmcnt(10)
	v_pk_add_f32 v[68:69], v[68:69], 1.0 op_sel_hi:[1,0]
	v_pk_add_f32 v[70:71], v[70:71], 1.0 op_sel_hi:[1,0]
	s_waitcnt vmcnt(9)
	v_pk_fma_f32 v[190:191], v[244:245], v[68:69], v[72:73]
	v_pk_fma_f32 v[188:189], v[188:189], v[70:71], v[74:75]
	v_cvt_pk_bf16_f32 v244, v190, v191
	v_pk_mul_f32 v[64:65], v[184:185], v[64:65]
	v_lshlrev_b32_e32 v246, 16, v244
	v_and_b32_e32 v247, 0xffff0000, v244
	v_sub_f32_e32 v246, v190, v246
	v_sub_f32_e32 v247, v191, v247
	v_cvt_pk_bf16_f32 v245, v188, v189
	v_cvt_pk_bf16_f32 v246, v246, v247
	v_pk_mul_f32 v[184:185], v[186:187], v[66:67]
	v_lshlrev_b32_e32 v247, 16, v245
	v_and_b32_e32 v249, 0xffff0000, v245
	v_sub_f32_e32 v247, v188, v247
	v_sub_f32_e32 v249, v189, v249
	v_cvt_pk_bf16_f32 v247, v247, v249
	v_xor_b32_e32 v249, s27, v248
	v_lshlrev_b32_e32 v249, 4, v249
	v_add3_u32 v249, s28, v249, v207
	ds_write_b64 v249, v[244:245]
	v_add_u32_e32 v244, 0x10000, v249
	ds_write_b64 v244, v[246:247]
	v_pk_fma_f32 v[186:187], v[64:65], v[68:69], v[72:73]
	v_pk_fma_f32 v[184:185], v[184:185], v[70:71], v[74:75]
	v_cvt_pk_bf16_f32 v192, v186, v187
	v_lshlrev_b64 v[200:201], 2, v[220:221]
	v_lshlrev_b32_e32 v194, 16, v192
	v_and_b32_e32 v195, 0xffff0000, v192
	v_sub_f32_e32 v194, v186, v194
	v_sub_f32_e32 v195, v187, v195
	v_cvt_pk_bf16_f32 v193, v184, v185
	v_cvt_pk_bf16_f32 v194, v194, v195
	v_add_u32_e32 v249, 32, v248
	v_lshlrev_b32_e32 v195, 16, v193
	v_and_b32_e32 v196, 0xffff0000, v193
	v_sub_f32_e32 v195, v184, v195
	v_sub_f32_e32 v196, v185, v196
	v_cvt_pk_bf16_f32 v195, v195, v196
	v_xor_b32_e32 v196, s29, v248
	v_lshlrev_b32_e32 v196, 4, v196
	v_add3_u32 v196, s30, v196, v207
	ds_write_b64 v196, v[192:193]
	v_add_u32_e32 v192, 0x10000, v196
	ds_write_b64 v192, v[194:195]
	v_lshl_add_u64 v[192:193], s[8:9], 0, v[200:201]
	v_lshl_add_u64 v[196:197], s[18:19], 0, v[200:201]
	global_load_dwordx4 v[64:67], v113, s[8:9]
	global_load_dwordx4 v[68:71], v113, s[18:19]
	global_load_dwordx4 v[72:75], v113, s[16:17]
	v_lshl_add_u64 v[200:201], s[16:17], 0, v[200:201]
	s_waitcnt vmcnt(11)
	v_pk_mul_f32 v[244:245], v[180:181], v[76:77]
	s_waitcnt vmcnt(10)
	v_pk_add_f32 v[80:81], v[80:81], 1.0 op_sel_hi:[1,0]
	v_pk_mul_f32 v[180:181], v[182:183], v[78:79]
	v_pk_add_f32 v[82:83], v[82:83], 1.0 op_sel_hi:[1,0]
	v_pk_mul_f32 v[76:77], v[176:177], v[76:77]
	v_pk_mul_f32 v[176:177], v[178:179], v[78:79]
	s_waitcnt vmcnt(9)
	v_pk_fma_f32 v[182:183], v[244:245], v[80:81], v[84:85]
	s_nop 0
	v_cvt_pk_bf16_f32 v244, v182, v183
	v_pk_fma_f32 v[180:181], v[180:181], v[82:83], v[86:87]
	v_lshlrev_b32_e32 v246, 16, v244
	v_and_b32_e32 v247, 0xffff0000, v244
	v_sub_f32_e32 v246, v182, v246
	v_sub_f32_e32 v247, v183, v247
	v_cvt_pk_bf16_f32 v245, v180, v181
	v_cvt_pk_bf16_f32 v246, v246, v247
	v_pk_fma_f32 v[178:179], v[76:77], v[80:81], v[84:85]
	v_lshlrev_b32_e32 v247, 16, v245
	v_and_b32_e32 v250, 0xffff0000, v245
	v_sub_f32_e32 v247, v180, v247
	v_sub_f32_e32 v250, v181, v250
	v_cvt_pk_bf16_f32 v247, v247, v250
	v_xor_b32_e32 v250, s27, v249
	v_lshlrev_b32_e32 v250, 4, v250
	v_add3_u32 v250, s28, v250, v207
	ds_write_b64 v250, v[244:245]
	v_add_u32_e32 v244, 0x10000, v250
	ds_write_b64 v244, v[246:247]
	v_cvt_pk_bf16_f32 v192, v178, v179
	v_pk_fma_f32 v[176:177], v[176:177], v[82:83], v[86:87]
	v_lshlrev_b32_e32 v194, 16, v192
	v_and_b32_e32 v195, 0xffff0000, v192
	v_sub_f32_e32 v194, v178, v194
	v_sub_f32_e32 v195, v179, v195
	v_cvt_pk_bf16_f32 v193, v176, v177
	v_cvt_pk_bf16_f32 v194, v194, v195
	v_lshlrev_b64 v[200:201], 2, v[218:219]
	v_lshlrev_b32_e32 v195, 16, v193
	v_and_b32_e32 v196, 0xffff0000, v193
	v_sub_f32_e32 v195, v176, v195
	v_sub_f32_e32 v196, v177, v196
	v_cvt_pk_bf16_f32 v195, v195, v196
	v_xor_b32_e32 v196, s29, v249
	v_lshlrev_b32_e32 v196, 4, v196
	v_add3_u32 v196, s30, v196, v207
	ds_write_b64 v196, v[192:193]
	v_add_u32_e32 v192, 0x10000, v196
	ds_write_b64 v192, v[194:195]
	v_lshl_add_u64 v[192:193], s[8:9], 0, v[200:201]
	v_lshl_add_u64 v[196:197], s[18:19], 0, v[200:201]
	global_load_dwordx4 v[76:79], v113, s[8:9] offset:1024
	global_load_dwordx4 v[80:83], v113, s[18:19] offset:1024
	global_load_dwordx4 v[84:87], v113, s[16:17] offset:1024
	v_lshl_add_u64 v[200:201], s[16:17], 0, v[200:201]
	v_add_u32_e32 v249, 64, v248
	s_waitcnt vmcnt(11)
	v_pk_mul_f32 v[244:245], v[172:173], v[88:89]
	v_pk_mul_f32 v[172:173], v[174:175], v[90:91]
	s_waitcnt vmcnt(10)
	v_pk_add_f32 v[92:93], v[92:93], 1.0 op_sel_hi:[1,0]
	v_pk_add_f32 v[94:95], v[94:95], 1.0 op_sel_hi:[1,0]
	s_waitcnt vmcnt(9)
	v_pk_fma_f32 v[174:175], v[244:245], v[92:93], v[96:97]
	v_pk_fma_f32 v[172:173], v[172:173], v[94:95], v[98:99]
	v_cvt_pk_bf16_f32 v244, v174, v175
	v_pk_mul_f32 v[88:89], v[168:169], v[88:89]
	v_lshlrev_b32_e32 v246, 16, v244
	v_and_b32_e32 v247, 0xffff0000, v244
	v_sub_f32_e32 v246, v174, v246
	v_sub_f32_e32 v247, v175, v247
	v_cvt_pk_bf16_f32 v245, v172, v173
	v_cvt_pk_bf16_f32 v246, v246, v247
	v_pk_mul_f32 v[168:169], v[170:171], v[90:91]
	v_lshlrev_b32_e32 v247, 16, v245
	v_and_b32_e32 v250, 0xffff0000, v245
	v_sub_f32_e32 v247, v172, v247
	v_sub_f32_e32 v250, v173, v250
	v_cvt_pk_bf16_f32 v247, v247, v250
	v_xor_b32_e32 v250, s27, v249
	v_lshlrev_b32_e32 v250, 4, v250
	v_add3_u32 v250, s28, v250, v207
	ds_write_b64 v250, v[244:245]
	v_add_u32_e32 v244, 0x10000, v250
	ds_write_b64 v244, v[246:247]
	v_pk_fma_f32 v[170:171], v[88:89], v[92:93], v[96:97]
	v_pk_fma_f32 v[168:169], v[168:169], v[94:95], v[98:99]
	v_cvt_pk_bf16_f32 v192, v170, v171
	v_lshlrev_b64 v[200:201], 2, v[216:217]
	v_lshlrev_b32_e32 v194, 16, v192
	v_and_b32_e32 v195, 0xffff0000, v192
	v_sub_f32_e32 v194, v170, v194
	v_sub_f32_e32 v195, v171, v195
	v_cvt_pk_bf16_f32 v193, v168, v169
	v_cvt_pk_bf16_f32 v194, v194, v195
	s_nop 0
	v_lshlrev_b32_e32 v195, 16, v193
	v_and_b32_e32 v196, 0xffff0000, v193
	v_sub_f32_e32 v195, v168, v195
	v_sub_f32_e32 v196, v169, v196
	v_cvt_pk_bf16_f32 v195, v195, v196
	v_xor_b32_e32 v196, s29, v249
	v_lshlrev_b32_e32 v196, 4, v196
	v_add3_u32 v196, s30, v196, v207
	ds_write_b64 v196, v[192:193]
	v_add_u32_e32 v192, 0x10000, v196
	ds_write_b64 v192, v[194:195]
	v_lshl_add_u64 v[192:193], s[8:9], 0, v[200:201]
	v_lshl_add_u64 v[196:197], s[18:19], 0, v[200:201]
	global_load_dwordx4 v[88:91], v113, s[8:9] offset:2048
	global_load_dwordx4 v[92:95], v113, s[18:19] offset:2048
	global_load_dwordx4 v[96:99], v113, s[16:17] offset:2048
	v_lshl_add_u64 v[200:201], s[16:17], 0, v[200:201]
	v_add_u32_e32 v249, 0x60, v248
	s_waitcnt vmcnt(11)
	v_pk_mul_f32 v[244:245], v[164:165], v[100:101]
	v_pk_mul_f32 v[164:165], v[166:167], v[102:103]
	s_waitcnt vmcnt(10)
	v_pk_add_f32 v[104:105], v[104:105], 1.0 op_sel_hi:[1,0]
	v_pk_add_f32 v[106:107], v[106:107], 1.0 op_sel_hi:[1,0]
	s_waitcnt vmcnt(9)
	v_pk_fma_f32 v[166:167], v[244:245], v[104:105], v[108:109]
	v_pk_fma_f32 v[164:165], v[164:165], v[106:107], v[110:111]
	v_cvt_pk_bf16_f32 v244, v166, v167
	v_pk_mul_f32 v[100:101], v[160:161], v[100:101]
	v_lshlrev_b32_e32 v246, 16, v244
	v_and_b32_e32 v247, 0xffff0000, v244
	v_sub_f32_e32 v246, v166, v246
	v_sub_f32_e32 v247, v167, v247
	v_cvt_pk_bf16_f32 v245, v164, v165
	v_cvt_pk_bf16_f32 v246, v246, v247
	v_pk_mul_f32 v[160:161], v[162:163], v[102:103]
	v_lshlrev_b32_e32 v247, 16, v245
	v_and_b32_e32 v250, 0xffff0000, v245
	v_sub_f32_e32 v247, v164, v247
	v_sub_f32_e32 v250, v165, v250
	v_cvt_pk_bf16_f32 v247, v247, v250
	v_xor_b32_e32 v250, s27, v249
	v_lshlrev_b32_e32 v250, 4, v250
	v_add3_u32 v250, s28, v250, v207
	ds_write_b64 v250, v[244:245]
	v_add_u32_e32 v244, 0x10000, v250
	ds_write_b64 v244, v[246:247]
	v_pk_fma_f32 v[162:163], v[100:101], v[104:105], v[108:109]
	v_pk_fma_f32 v[160:161], v[160:161], v[106:107], v[110:111]
	v_cvt_pk_bf16_f32 v192, v162, v163
	v_lshlrev_b64 v[200:201], 2, v[214:215]
	v_lshlrev_b32_e32 v194, 16, v192
	v_and_b32_e32 v195, 0xffff0000, v192
	v_sub_f32_e32 v194, v162, v194
	v_sub_f32_e32 v195, v163, v195
	v_cvt_pk_bf16_f32 v193, v160, v161
	v_cvt_pk_bf16_f32 v194, v194, v195
	s_nop 0
	v_lshlrev_b32_e32 v195, 16, v193
	v_and_b32_e32 v196, 0xffff0000, v193
	v_sub_f32_e32 v195, v160, v195
	v_sub_f32_e32 v196, v161, v196
	v_cvt_pk_bf16_f32 v195, v195, v196
	v_xor_b32_e32 v196, s29, v249
	v_lshlrev_b32_e32 v196, 4, v196
	v_add3_u32 v196, s30, v196, v207
	ds_write_b64 v196, v[192:193]
	v_add_u32_e32 v192, 0x10000, v196
	ds_write_b64 v192, v[194:195]
	v_lshl_add_u64 v[192:193], s[8:9], 0, v[200:201]
	v_lshl_add_u64 v[196:197], s[18:19], 0, v[200:201]
	global_load_dwordx4 v[100:103], v113, s[8:9] offset:3072
	global_load_dwordx4 v[104:107], v113, s[18:19] offset:3072
	global_load_dwordx4 v[108:111], v113, s[16:17] offset:3072
	v_lshl_add_u64 v[200:201], s[16:17], 0, v[200:201]
	v_add_u32_e32 v249, 0x80, v248
	s_waitcnt vmcnt(11)
	v_pk_mul_f32 v[244:245], v[156:157], v[64:65]
	v_pk_mul_f32 v[156:157], v[158:159], v[66:67]
	s_waitcnt vmcnt(10)
	v_pk_add_f32 v[68:69], v[68:69], 1.0 op_sel_hi:[1,0]
	v_pk_add_f32 v[70:71], v[70:71], 1.0 op_sel_hi:[1,0]
	s_waitcnt vmcnt(9)
	v_pk_fma_f32 v[158:159], v[244:245], v[68:69], v[72:73]
	v_pk_fma_f32 v[156:157], v[156:157], v[70:71], v[74:75]
	v_cvt_pk_bf16_f32 v244, v158, v159
	v_pk_mul_f32 v[64:65], v[152:153], v[64:65]
	v_lshlrev_b32_e32 v246, 16, v244
	v_and_b32_e32 v247, 0xffff0000, v244
	v_sub_f32_e32 v246, v158, v246
	v_sub_f32_e32 v247, v159, v247
	v_cvt_pk_bf16_f32 v245, v156, v157
	v_cvt_pk_bf16_f32 v246, v246, v247
	v_pk_mul_f32 v[152:153], v[154:155], v[66:67]
	v_lshlrev_b32_e32 v247, 16, v245
	v_and_b32_e32 v250, 0xffff0000, v245
	v_sub_f32_e32 v247, v156, v247
	v_sub_f32_e32 v250, v157, v250
	v_cvt_pk_bf16_f32 v247, v247, v250
	v_xor_b32_e32 v250, s27, v249
	v_lshlrev_b32_e32 v250, 4, v250
	v_add3_u32 v250, s28, v250, v207
	ds_write_b64 v250, v[244:245]
	v_add_u32_e32 v244, 0x10000, v250
	ds_write_b64 v244, v[246:247]
	v_pk_fma_f32 v[154:155], v[64:65], v[68:69], v[72:73]
	v_pk_fma_f32 v[152:153], v[152:153], v[70:71], v[74:75]
	v_cvt_pk_bf16_f32 v192, v154, v155
	v_lshlrev_b64 v[200:201], 2, v[212:213]
	v_lshlrev_b32_e32 v194, 16, v192
	v_and_b32_e32 v195, 0xffff0000, v192
	v_sub_f32_e32 v194, v154, v194
	v_sub_f32_e32 v195, v155, v195
	v_cvt_pk_bf16_f32 v193, v152, v153
	v_cvt_pk_bf16_f32 v194, v194, v195
	s_nop 0
	v_lshlrev_b32_e32 v195, 16, v193
	v_and_b32_e32 v196, 0xffff0000, v193
	v_sub_f32_e32 v195, v152, v195
	v_sub_f32_e32 v196, v153, v196
	v_cvt_pk_bf16_f32 v195, v195, v196
	v_xor_b32_e32 v196, s29, v249
	v_lshlrev_b32_e32 v196, 4, v196
	v_add3_u32 v196, s30, v196, v207
	ds_write_b64 v196, v[192:193]
	v_add_u32_e32 v192, 0x10000, v196
	ds_write_b64 v192, v[194:195]
	v_lshl_add_u64 v[192:193], s[8:9], 0, v[200:201]
	v_lshl_add_u64 v[196:197], s[18:19], 0, v[200:201]
	v_lshl_add_u64 v[200:201], s[16:17], 0, v[200:201]
	v_add_u32_e32 v249, 0xa0, v248
	s_waitcnt vmcnt(8)
	v_pk_mul_f32 v[244:245], v[148:149], v[76:77]
	v_pk_mul_f32 v[148:149], v[150:151], v[78:79]
	s_waitcnt vmcnt(7)
	v_pk_add_f32 v[80:81], v[80:81], 1.0 op_sel_hi:[1,0]
	v_pk_add_f32 v[82:83], v[82:83], 1.0 op_sel_hi:[1,0]
	s_waitcnt vmcnt(6)
	v_pk_fma_f32 v[150:151], v[244:245], v[80:81], v[84:85]
	v_pk_fma_f32 v[148:149], v[148:149], v[82:83], v[86:87]
	v_cvt_pk_bf16_f32 v244, v150, v151
	v_pk_mul_f32 v[76:77], v[144:145], v[76:77]
	v_lshlrev_b32_e32 v246, 16, v244
	v_and_b32_e32 v247, 0xffff0000, v244
	v_sub_f32_e32 v246, v150, v246
	v_sub_f32_e32 v247, v151, v247
	v_cvt_pk_bf16_f32 v245, v148, v149
	v_cvt_pk_bf16_f32 v246, v246, v247
	v_pk_mul_f32 v[144:145], v[146:147], v[78:79]
	v_lshlrev_b32_e32 v247, 16, v245
	v_and_b32_e32 v250, 0xffff0000, v245
	v_sub_f32_e32 v247, v148, v247
	v_sub_f32_e32 v250, v149, v250
	v_cvt_pk_bf16_f32 v247, v247, v250
	v_xor_b32_e32 v250, s27, v249
	v_lshlrev_b32_e32 v250, 4, v250
	v_add3_u32 v250, s28, v250, v207
	ds_write_b64 v250, v[244:245]
	v_add_u32_e32 v244, 0x10000, v250
	ds_write_b64 v244, v[246:247]
	v_pk_fma_f32 v[146:147], v[76:77], v[80:81], v[84:85]
	v_pk_fma_f32 v[144:145], v[144:145], v[82:83], v[86:87]
	v_cvt_pk_bf16_f32 v192, v146, v147
	v_lshlrev_b64 v[200:201], 2, v[210:211]
	v_lshlrev_b32_e32 v194, 16, v192
	v_and_b32_e32 v195, 0xffff0000, v192
	v_sub_f32_e32 v194, v146, v194
	v_sub_f32_e32 v195, v147, v195
	v_cvt_pk_bf16_f32 v193, v144, v145
	v_cvt_pk_bf16_f32 v194, v194, v195
	s_nop 0
	v_lshlrev_b32_e32 v195, 16, v193
	v_and_b32_e32 v196, 0xffff0000, v193
	v_sub_f32_e32 v195, v144, v195
	v_sub_f32_e32 v196, v145, v196
	v_cvt_pk_bf16_f32 v195, v195, v196
	v_xor_b32_e32 v196, s29, v249
	v_lshlrev_b32_e32 v196, 4, v196
	v_add3_u32 v196, s30, v196, v207
	ds_write_b64 v196, v[192:193]
	v_add_u32_e32 v192, 0x10000, v196
	ds_write_b64 v192, v[194:195]
	v_lshl_add_u64 v[192:193], s[8:9], 0, v[200:201]
	v_lshl_add_u64 v[196:197], s[18:19], 0, v[200:201]
	v_lshl_add_u64 v[200:201], s[16:17], 0, v[200:201]
	v_add_u32_e32 v249, 0xc0, v248
	v_add_u32_e32 v248, 0xe0, v248
	s_waitcnt vmcnt(5)
	v_pk_mul_f32 v[244:245], v[140:141], v[88:89]
	v_pk_mul_f32 v[140:141], v[142:143], v[90:91]
	s_waitcnt vmcnt(4)
	v_pk_add_f32 v[92:93], v[92:93], 1.0 op_sel_hi:[1,0]
	v_pk_add_f32 v[94:95], v[94:95], 1.0 op_sel_hi:[1,0]
	s_waitcnt vmcnt(3)
	v_pk_fma_f32 v[142:143], v[244:245], v[92:93], v[96:97]
	v_pk_fma_f32 v[140:141], v[140:141], v[94:95], v[98:99]
	v_cvt_pk_bf16_f32 v244, v142, v143
	v_pk_mul_f32 v[88:89], v[136:137], v[88:89]
	v_lshlrev_b32_e32 v246, 16, v244
	v_and_b32_e32 v247, 0xffff0000, v244
	v_sub_f32_e32 v246, v142, v246
	v_sub_f32_e32 v247, v143, v247
	v_cvt_pk_bf16_f32 v245, v140, v141
	v_cvt_pk_bf16_f32 v246, v246, v247
	v_pk_mul_f32 v[136:137], v[138:139], v[90:91]
	v_lshlrev_b32_e32 v247, 16, v245
	v_and_b32_e32 v250, 0xffff0000, v245
	v_sub_f32_e32 v247, v140, v247
	v_sub_f32_e32 v250, v141, v250
	v_cvt_pk_bf16_f32 v247, v247, v250
	v_xor_b32_e32 v250, s27, v249
	v_lshlrev_b32_e32 v250, 4, v250
	v_add3_u32 v250, s28, v250, v207
	ds_write_b64 v250, v[244:245]
	v_add_u32_e32 v244, 0x10000, v250
	ds_write_b64 v244, v[246:247]
	v_pk_fma_f32 v[138:139], v[88:89], v[92:93], v[96:97]
	v_pk_fma_f32 v[136:137], v[136:137], v[94:95], v[98:99]
	v_cvt_pk_bf16_f32 v192, v138, v139
	v_lshlrev_b64 v[200:201], 2, v[208:209]
	v_lshlrev_b32_e32 v194, 16, v192
	v_and_b32_e32 v195, 0xffff0000, v192
	v_sub_f32_e32 v194, v138, v194
	v_sub_f32_e32 v195, v139, v195
	v_cvt_pk_bf16_f32 v193, v136, v137
	v_cvt_pk_bf16_f32 v194, v194, v195
	s_nop 0
	v_lshlrev_b32_e32 v195, 16, v193
	v_and_b32_e32 v196, 0xffff0000, v193
	v_sub_f32_e32 v195, v136, v195
	v_sub_f32_e32 v196, v137, v196
	v_cvt_pk_bf16_f32 v195, v195, v196
	v_xor_b32_e32 v196, s29, v249
	v_lshlrev_b32_e32 v196, 4, v196
	v_add3_u32 v196, s30, v196, v207
	ds_write_b64 v196, v[192:193]
	v_add_u32_e32 v192, 0x10000, v196
	ds_write_b64 v192, v[194:195]
	v_lshl_add_u64 v[192:193], s[8:9], 0, v[200:201]
	v_lshl_add_u64 v[196:197], s[18:19], 0, v[200:201]
	v_lshl_add_u64 v[200:201], s[16:17], 0, v[200:201]
	s_lshl_b64 s[16:17], s[12:13], 11
	s_add_u32 s16, s23, s16
	s_addc_u32 s17, s24, s17
	s_lshl_b64 s[4:5], s[4:5], 11
	s_add_u32 s4, s23, s4
	s_addc_u32 s5, s24, s5
	s_waitcnt vmcnt(2)
	v_pk_mul_f32 v[244:245], v[132:133], v[100:101]
	v_pk_mul_f32 v[132:133], v[134:135], v[102:103]
	s_waitcnt vmcnt(1)
	v_pk_add_f32 v[104:105], v[104:105], 1.0 op_sel_hi:[1,0]
	v_pk_add_f32 v[106:107], v[106:107], 1.0 op_sel_hi:[1,0]
	s_waitcnt vmcnt(0)
	v_pk_fma_f32 v[134:135], v[244:245], v[104:105], v[108:109]
	v_pk_fma_f32 v[132:133], v[132:133], v[106:107], v[110:111]
	v_cvt_pk_bf16_f32 v244, v134, v135
	v_pk_mul_f32 v[100:101], v[128:129], v[100:101]
	v_lshlrev_b32_e32 v204, 16, v244
	v_and_b32_e32 v246, 0xffff0000, v244
	v_sub_f32_e32 v204, v134, v204
	v_sub_f32_e32 v246, v135, v246
	v_cvt_pk_bf16_f32 v245, v132, v133
	v_cvt_pk_bf16_f32 v246, v204, v246
	v_pk_mul_f32 v[128:129], v[130:131], v[102:103]
	v_lshlrev_b32_e32 v204, 16, v245
	v_and_b32_e32 v247, 0xffff0000, v245
	v_sub_f32_e32 v204, v132, v204
	v_sub_f32_e32 v247, v133, v247
	v_cvt_pk_bf16_f32 v247, v204, v247
	v_xor_b32_e32 v204, s27, v248
	v_lshlrev_b32_e32 v204, 4, v204
	v_add3_u32 v204, s28, v204, v207
	ds_write_b64 v204, v[244:245]
	v_add_u32_e32 v204, 0x10000, v204
	ds_write_b64 v204, v[246:247]
	v_pk_fma_f32 v[130:131], v[100:101], v[104:105], v[108:109]
	v_pk_fma_f32 v[128:129], v[128:129], v[106:107], v[110:111]
	s_cmp_lt_i32 s41, s44
	s_cbranch_scc0 .Lpf_skip_g
	s_add_i32 s98, s33, s12
	s_ashr_i32 s99, s98, 31
	s_lshl_b64 s[98:99], s[98:99], 13
	s_add_u32 s98, s6, s98
	s_addc_u32 s99, s7, s99
	v_lshlrev_b64 v[96:97], 2, v[222:223]
	v_lshlrev_b64 v[112:113], 2, v[214:215]
	v_lshlrev_b64 v[114:115], 2, v[212:213]
	v_lshlrev_b64 v[120:121], 2, v[210:211]
	v_lshlrev_b64 v[122:123], 2, v[208:209]
	v_lshl_add_u64 v[76:77], s[98:99], 0, v[96:97]
	v_lshl_add_u64 v[80:81], s[98:99], 0, v[112:113]
	v_lshl_add_u64 v[84:85], s[98:99], 0, v[114:115]
	v_lshl_add_u64 v[88:89], s[98:99], 0, v[120:121]
	v_lshl_add_u64 v[92:93], s[98:99], 0, v[122:123]
	s_add_i32 s98, s31, s12
	s_ashr_i32 s99, s98, 31
	s_lshl_b64 s[98:99], s[98:99], 13
	s_add_u32 s98, s6, s98
	s_addc_u32 s99, s7, s99
	v_lshl_add_u64 v[108:109], s[98:99], 0, v[96:97]
	global_load_dwordx4 v[64:67], v[76:77], off
	global_load_dwordx4 v[68:71], v[76:77], off offset:1024
	global_load_dwordx4 v[72:75], v[76:77], off offset:2048
	s_nop 0
	global_load_dwordx4 v[76:79], v[76:77], off offset:3072
	s_nop 0
	global_load_dwordx4 v[80:83], v[80:81], off
	s_nop 0
	global_load_dwordx4 v[84:87], v[84:85], off
	s_nop 0
	global_load_dwordx4 v[88:91], v[88:89], off
	s_nop 0
	global_load_dwordx4 v[92:95], v[92:93], off
	s_nop 0
	global_load_dwordx4 v[96:99], v[108:109], off
	global_load_dwordx4 v[100:103], v[108:109], off offset:1024
	global_load_dwordx4 v[104:107], v[108:109], off offset:2048
	s_nop 0
	global_load_dwordx4 v[108:111], v[108:109], off offset:3072
	v_lshl_add_u64 v[112:113], s[98:99], 0, v[112:113]
	v_lshl_add_u64 v[116:117], s[98:99], 0, v[114:115]
	v_lshl_add_u64 v[120:121], s[98:99], 0, v[120:121]
	v_lshl_add_u64 v[124:125], s[98:99], 0, v[122:123]
	global_load_dwordx4 v[112:115], v[112:113], off
	s_nop 0
	global_load_dwordx4 v[116:119], v[116:117], off
	s_nop 0
	global_load_dwordx4 v[120:123], v[120:121], off
	s_nop 0
	global_load_dwordx4 v[124:127], v[124:125], off

.LBB0_1741:
	v_cvt_pk_f32_fp8_e32 v[152:153], v146
	v_cvt_pk_f32_fp8_sdwa v[156:157], v146 src0_sel:WORD_1
	v_lshlrev_b32_e32 v146, 16, v130
	v_and_b32_e32 v147, 0xffff0000, v130
	v_lshlrev_b32_e32 v130, 16, v131
	v_and_b32_e32 v131, 0xffff0000, v131
	v_pk_add_f32 v[146:147], v[152:153], v[146:147]
	v_pk_add_f32 v[152:153], v[156:157], v[130:131]
	v_cvt_pk_f32_fp8_e32 v[130:131], v150
	v_cvt_pk_f32_fp8_sdwa v[150:151], v150 src0_sel:WORD_1
	v_lshlrev_b32_e32 v156, 16, v94
	v_and_b32_e32 v157, 0xffff0000, v94
	v_lshlrev_b32_e32 v94, 16, v95
	v_and_b32_e32 v95, 0xffff0000, v95
	v_pk_add_f32 v[164:165], v[150:151], v[94:95]
	v_cvt_pk_f32_fp8_e32 v[94:95], v149
	v_cvt_pk_f32_fp8_e32 v[150:151], v148
	v_pk_add_f32 v[162:163], v[130:131], v[156:157]
	v_cvt_pk_f32_fp8_sdwa v[130:131], v149 src0_sel:WORD_1
	v_cvt_pk_f32_fp8_sdwa v[158:159], v148 src0_sel:WORD_1
	v_lshlrev_b32_e32 v149, 16, v92
	v_lshlrev_b32_e32 v148, 16, v84
	v_mov_b32_e32 v156, v94
	v_mov_b32_e32 v157, v150
	v_pk_add_f32 v[148:149], v[156:157], v[148:149]
	v_and_b32_e32 v157, 0xffff0000, v92
	v_and_b32_e32 v156, 0xffff0000, v84
	v_mov_b32_e32 v150, v95
	v_pk_add_f32 v[150:151], v[150:151], v[156:157]
	v_lshlrev_b32_e32 v95, 16, v93
	v_lshlrev_b32_e32 v94, 16, v85
	v_mov_b32_e32 v156, v130
	v_mov_b32_e32 v157, v158
	v_pk_add_f32 v[156:157], v[156:157], v[94:95]
	v_and_b32_e32 v92, 0xffff0000, v85
	v_cvt_pk_f32_fp8_e32 v[84:85], v135
	v_cvt_pk_f32_fp8_e32 v[94:95], v134
	v_cvt_pk_f32_fp8_sdwa v[174:175], v135 src0_sel:WORD_1
	v_cvt_pk_f32_fp8_sdwa v[134:135], v134 src0_sel:WORD_1
	v_and_b32_e32 v93, 0xffff0000, v93
	v_mov_b32_e32 v158, v131
	v_pk_add_f32 v[158:159], v[158:159], v[92:93]
	v_lshlrev_b32_e32 v93, 16, v82
	v_lshlrev_b32_e32 v92, 16, v80
	v_mov_b32_e32 v130, v84
	v_mov_b32_e32 v131, v94
	v_pk_add_f32 v[92:93], v[130:131], v[92:93]
	v_and_b32_e32 v131, 0xffff0000, v82
	v_and_b32_e32 v130, 0xffff0000, v80
	v_mov_b32_e32 v94, v85
	v_pk_add_f32 v[94:95], v[94:95], v[130:131]
	v_lshlrev_b32_e32 v85, 16, v83
	v_lshlrev_b32_e32 v84, 16, v81
	v_mov_b32_e32 v130, v174
	v_mov_b32_e32 v131, v134
	v_and_b32_e32 v83, 0xffff0000, v83
	v_and_b32_e32 v82, 0xffff0000, v81
	v_mov_b32_e32 v134, v175
	v_pk_add_f32 v[130:131], v[130:131], v[84:85]
	v_pk_add_f32 v[134:135], v[134:135], v[82:83]
	v_cvt_pk_f32_fp8_e32 v[82:83], v173
	v_cvt_pk_f32_fp8_e32 v[84:85], v171
	v_cvt_pk_f32_fp8_sdwa v[174:175], v173 src0_sel:WORD_1
	v_cvt_pk_f32_fp8_sdwa v[176:177], v171 src0_sel:WORD_1
	v_lshlrev_b32_e32 v81, 16, v144
	v_lshlrev_b32_e32 v80, 16, v86
	v_mov_b32_e32 v178, v82
	v_mov_b32_e32 v179, v84
	v_pk_add_f32 v[80:81], v[178:179], v[80:81]
	v_and_b32_e32 v179, 0xffff0000, v144
	v_and_b32_e32 v178, 0xffff0000, v86
	v_mov_b32_e32 v84, v83
	v_pk_add_f32 v[82:83], v[84:85], v[178:179]
	v_lshlrev_b32_e32 v85, 16, v145
	v_mov_b32_e32 v179, v176
	v_and_b32_e32 v145, 0xffff0000, v145
	v_and_b32_e32 v144, 0xffff0000, v87
	v_mov_b32_e32 v176, v175
	v_lshlrev_b32_e32 v84, 16, v87
	v_pk_add_f32 v[86:87], v[176:177], v[144:145]
	v_cvt_pk_f32_fp8_e32 v[144:145], v170
	v_mov_b32_e32 v178, v174
	v_cvt_pk_f32_fp8_sdwa v[174:175], v170 src0_sel:WORD_1
	v_lshlrev_b32_e32 v170, 16, v142
	v_and_b32_e32 v171, 0xffff0000, v142
	v_pk_add_f32 v[170:171], v[144:145], v[170:171]
	v_cvt_pk_f32_fp8_sdwa v[144:145], v172 src0_sel:WORD_1
	v_lshlrev_b32_e32 v142, 16, v143
	v_and_b32_e32 v143, 0xffff0000, v143
	v_pk_add_f32 v[174:175], v[174:175], v[142:143]
	v_cvt_pk_f32_fp8_e32 v[142:143], v172
	v_lshlrev_b32_e32 v172, 16, v140
	v_and_b32_e32 v173, 0xffff0000, v140
	v_lshlrev_b32_e32 v140, 16, v141
	v_and_b32_e32 v141, 0xffff0000, v141
	v_pk_add_f32 v[182:183], v[144:145], v[140:141]
	v_cvt_pk_f32_fp8_e32 v[140:141], v169
	v_cvt_pk_f32_fp8_e32 v[144:145], v168
	v_pk_add_f32 v[84:85], v[178:179], v[84:85]
	v_pk_add_f32 v[180:181], v[142:143], v[172:173]
	v_cvt_pk_f32_fp8_sdwa v[142:143], v169 src0_sel:WORD_1
	v_cvt_pk_f32_fp8_sdwa v[178:179], v168 src0_sel:WORD_1
	v_lshlrev_b32_e32 v169, 16, v138
	v_lshlrev_b32_e32 v168, 16, v128
	v_mov_b32_e32 v172, v140
	v_mov_b32_e32 v173, v144
	v_pk_add_f32 v[168:169], v[172:173], v[168:169]
	v_and_b32_e32 v173, 0xffff0000, v138
	v_and_b32_e32 v172, 0xffff0000, v128
	v_mov_b32_e32 v144, v141
	v_pk_add_f32 v[172:173], v[144:145], v[172:173]
	v_lshlrev_b32_e32 v141, 16, v139
	v_lshlrev_b32_e32 v140, 16, v129
	v_mov_b32_e32 v144, v142
	v_mov_b32_e32 v145, v178
	v_pk_add_f32 v[176:177], v[144:145], v[140:141]
	v_and_b32_e32 v138, 0xffff0000, v129
	v_cvt_pk_f32_fp8_e32 v[128:129], v166
	v_cvt_pk_f32_fp8_e32 v[140:141], v160
	v_cvt_pk_f32_fp8_sdwa v[144:145], v166 src0_sel:WORD_1
	v_cvt_pk_f32_fp8_sdwa v[184:185], v160 src0_sel:WORD_1
	v_and_b32_e32 v139, 0xffff0000, v139
	v_mov_b32_e32 v178, v143
	v_pk_add_f32 v[178:179], v[178:179], v[138:139]
	v_lshlrev_b32_e32 v139, 16, v90
	v_lshlrev_b32_e32 v138, 16, v88
	v_mov_b32_e32 v142, v128
	v_mov_b32_e32 v143, v140
	v_pk_add_f32 v[138:139], v[142:143], v[138:139]
	v_and_b32_e32 v143, 0xffff0000, v90
	v_and_b32_e32 v142, 0xffff0000, v88
	v_mov_b32_e32 v140, v129
	v_pk_add_f32 v[140:141], v[140:141], v[142:143]
	v_lshlrev_b32_e32 v129, 16, v91
	v_lshlrev_b32_e32 v128, 16, v89
	v_mov_b32_e32 v142, v144
	v_mov_b32_e32 v143, v184
	v_and_b32_e32 v91, 0xffff0000, v91
	v_and_b32_e32 v90, 0xffff0000, v89
	v_mov_b32_e32 v184, v145
	v_pk_add_f32 v[142:143], v[142:143], v[128:129]
	v_pk_add_f32 v[144:145], v[184:185], v[90:91]
	v_cvt_pk_f32_fp8_e32 v[90:91], v155
	v_cvt_pk_f32_fp8_e32 v[128:129], v154
	v_lshlrev_b32_e32 v89, 16, v136
	v_lshlrev_b32_e32 v88, 16, v132
	v_mov_b32_e32 v186, v90
	v_mov_b32_e32 v187, v128
	v_pk_mul_f32 v[228:229], v[146:147], v[146:147]
	v_pk_mul_f32 v[232:233], v[162:163], v[162:163]
	v_pk_add_f32 v[88:89], v[186:187], v[88:89]
	v_and_b32_e32 v187, 0xffff0000, v136
	v_and_b32_e32 v186, 0xffff0000, v132
	v_pk_mul_f32 v[230:231], v[152:153], v[152:153]
	v_pk_mul_f32 v[234:235], v[164:165], v[164:165]
	v_pk_mul_f32 v[236:237], v[150:151], v[150:151]
	v_add_f32_e32 v132, v232, v233
	v_add_f32_e32 v136, v228, v229
	v_pk_fma_f32 v[236:237], v[148:149], v[148:149], v[236:237]
	v_add_f32_e32 v132, v234, v132
	v_add_f32_e32 v136, v230, v136
	v_pk_fma_f32 v[236:237], v[156:157], v[156:157], v[236:237]
	v_pk_mul_f32 v[238:239], v[94:95], v[94:95]
	v_add_f32_e32 v132, v235, v132
	v_add_f32_e32 v136, v231, v136
	v_pk_fma_f32 v[236:237], v[158:159], v[158:159], v[236:237]
	v_pk_fma_f32 v[238:239], v[92:93], v[92:93], v[238:239]
	v_add_f32_e32 v132, v136, v132
	v_pk_fma_f32 v[238:239], v[130:131], v[130:131], v[238:239]
	v_pk_mul_f32 v[240:241], v[82:83], v[82:83]
	v_add_f32_e32 v132, v132, v236
	v_pk_fma_f32 v[238:239], v[134:135], v[134:135], v[238:239]
	v_pk_fma_f32 v[240:241], v[80:81], v[80:81], v[240:241]
	v_add_f32_e32 v132, v132, v237
	v_pk_fma_f32 v[240:241], v[84:85], v[84:85], v[240:241]
	v_add_f32_e32 v132, v132, v238
	v_pk_fma_f32 v[240:241], v[86:87], v[86:87], v[240:241]
	v_add_f32_e32 v132, v132, v239
	v_add_f32_e32 v132, v132, v240
	v_add_f32_e32 v132, v132, v241
	v_cvt_pk_f32_fp8_sdwa v[184:185], v155 src0_sel:WORD_1
	v_cvt_pk_f32_fp8_sdwa v[154:155], v154 src0_sel:WORD_1
	v_add_f32_dpp v132, v132, v132 quad_perm:[1,0,3,2] row_mask:0xf bank_mask:0xf bound_ctrl:1
	v_mov_b32_e32 v128, v91
	v_pk_add_f32 v[90:91], v[128:129], v[186:187]
	v_add_f32_dpp v132, v132, v132 quad_perm:[2,3,0,1] row_mask:0xf bank_mask:0xf bound_ctrl:1
	v_mov_b32_e32 v187, v154
	v_mov_b32_e32 v186, v184
	v_add_f32_dpp v132, v132, v132 row_half_mirror row_mask:0xf bank_mask:0xf bound_ctrl:1
	v_lshlrev_b64 v[234:235], 2, v[78:79]
	v_lshlrev_b32_e32 v129, 16, v137
	v_add_f32_dpp v132, v132, v132 row_mirror row_mask:0xf bank_mask:0xf bound_ctrl:1
	v_lshlrev_b32_e32 v128, 16, v133
	v_readlane_b32 s8, v132, 16
	v_readlane_b32 s9, v132, 48
	v_readlane_b32 s6, v132, 0
	v_readlane_b32 s7, v132, 32
	v_mov_b32_e32 v228, s8
	v_mov_b32_e32 v229, s9
	v_pk_add_f32 v[228:229], s[6:7], v[228:229]
	v_pk_add_f32 v[128:129], v[186:187], v[128:129]
	v_add_f32_e32 v132, v228, v229
	v_fmamk_f32 v132, v132, 0x3a000000, v206
	v_mul_f32_e32 v136, 0x4f800000, v132
	v_cmp_gt_f32_e32 vcc, s49, v132
	v_and_b32_e32 v137, 0xffff0000, v137
	v_pk_mul_f32 v[228:229], v[180:181], v[180:181]
	v_cndmask_b32_e32 v132, v132, v136, vcc
	v_sqrt_f32_e32 v136, v132
	v_pk_mul_f32 v[238:239], v[182:183], v[182:183]
	v_add_f32_e32 v228, v228, v229
	v_add_f32_e32 v228, v238, v228
	v_add_u32_e32 v154, -1, v136
	v_fma_f32 v160, -v154, v136, v132
	v_cmp_ge_f32_e64 s[6:7], 0, v160
	v_add_u32_e32 v160, 1, v136
	v_pk_mul_f32 v[242:243], v[140:141], v[140:141]
	v_cndmask_b32_e64 v154, v136, v154, s[6:7]
	v_fma_f32 v136, -v160, v136, v132
	v_cmp_lt_f32_e64 s[6:7], 0, v136
	v_add_f32_e32 v228, v239, v228
	v_pk_fma_f32 v[242:243], v[138:139], v[138:139], v[242:243]
	v_cndmask_b32_e64 v136, v154, v160, s[6:7]
	v_mul_f32_e32 v154, 0x37800000, v136
	v_cndmask_b32_e32 v136, v136, v154, vcc
	v_cmp_class_f32_e32 vcc, v132, v207
	v_mov_b32_e32 v154, v185
	v_pk_mul_f32 v[184:185], v[172:173], v[172:173]
	v_cndmask_b32_e32 v160, v136, v132, vcc
	v_div_scale_f32 v166, s[6:7], v160, v160, 1.0
	s_ashr_i32 s6, s18, 12
	s_mul_hi_i32 s7, s6, 0xc000
	s_mul_i32 s6, s6, 0xc000
	s_add_u32 s6, s2, s6
	s_addc_u32 s7, s3, s7
	s_add_u32 s10, s6, 0xe000
	s_addc_u32 s11, s7, 0
	v_pk_fma_f32 v[230:231], v[168:169], v[168:169], v[184:185]
	s_add_u32 s12, s6, 0x10000
	s_addc_u32 s13, s7, 0
	v_pk_fma_f32 v[230:231], v[176:177], v[176:177], v[230:231]
	v_lshl_add_u64 v[184:185], s[12:13], 0, v[234:235]
	v_pk_fma_f32 v[240:241], v[178:179], v[178:179], v[230:231]
	s_waitcnt lgkmcnt(0)
	v_lshl_add_u64 v[230:231], s[24:25], 0, v[234:235]
	v_lshlrev_b32_e32 v250, 4, v189
	v_add_u32_e32 v251, 0x1000, v250
	global_load_dwordx4 v[96:99], v250, s[12:13]
	global_load_dwordx4 v[100:103], v250, s[24:25]
	global_load_dwordx4 v[104:107], v250, s[10:11]
	global_load_dwordx4 v[108:111], v250, s[12:13] offset:1024
	global_load_dwordx4 v[112:115], v250, s[24:25] offset:1024
	global_load_dwordx4 v[116:119], v250, s[10:11] offset:1024
	global_load_dwordx4 v[120:123], v250, s[12:13] offset:2048
	global_load_dwordx4 v[124:127], v250, s[24:25] offset:2048
	global_load_dwordx4 v[212:215], v250, s[10:11] offset:2048
	global_load_dwordx4 v[216:219], v250, s[12:13] offset:3072
	global_load_dwordx4 v[220:223], v250, s[24:25] offset:3072
	global_load_dwordx4 v[224:227], v250, s[10:11] offset:3072
	v_lshl_add_u64 v[234:235], s[10:11], 0, v[234:235]
	v_rcp_f32_e32 v246, v166
	v_and_b32_e32 v136, 0xffff0000, v133
	v_pk_add_f32 v[132:133], v[154:155], v[136:137]
	v_fma_f32 v136, -v166, v246, 1.0
	v_fmac_f32_e32 v246, v136, v246
	v_pk_mul_f32 v[136:137], v[170:171], v[170:171]
	v_pk_mul_f32 v[154:155], v[174:175], v[174:175]
	v_add_f32_e32 v136, v136, v137
	v_add_f32_e32 v136, v154, v136
	v_add_f32_e32 v136, v155, v136
	v_add_f32_e32 v136, v136, v228
	v_pk_fma_f32 v[242:243], v[142:143], v[142:143], v[242:243]
	v_pk_mul_f32 v[244:245], v[90:91], v[90:91]
	v_add_f32_e32 v136, v136, v240
	v_pk_fma_f32 v[242:243], v[144:145], v[144:145], v[242:243]
	v_pk_fma_f32 v[244:245], v[88:89], v[88:89], v[244:245]
	v_add_f32_e32 v136, v136, v241
	v_pk_fma_f32 v[244:245], v[128:129], v[128:129], v[244:245]
	v_add_f32_e32 v136, v136, v242
	v_pk_fma_f32 v[244:245], v[132:133], v[132:133], v[244:245]
	v_add_f32_e32 v136, v136, v243
	v_add_f32_e32 v136, v136, v244
	v_add_f32_e32 v136, v136, v245
	v_div_scale_f32 v247, vcc, 1.0, v160, 1.0
	s_nop 0
	v_add_f32_dpp v136, v136, v136 quad_perm:[1,0,3,2] row_mask:0xf bank_mask:0xf bound_ctrl:1
	v_mul_f32_e32 v248, v247, v246
	v_fma_f32 v154, -v166, v248, v247
	v_add_f32_dpp v136, v136, v136 quad_perm:[2,3,0,1] row_mask:0xf bank_mask:0xf bound_ctrl:1
	v_fmac_f32_e32 v248, v154, v246
	v_fma_f32 v154, -v166, v248, v247
	v_add_f32_dpp v136, v136, v136 row_half_mirror row_mask:0xf bank_mask:0xf bound_ctrl:1
	v_div_fmas_f32 v154, v154, v246, v248
	v_lshrrev_b32_e32 v229, 1, v189
	v_add_f32_dpp v136, v136, v136 row_mirror row_mask:0xf bank_mask:0xf bound_ctrl:1
	v_add_u32_e32 v246, 64, v229
	v_readlane_b32 s8, v136, 16
	v_readlane_b32 s9, v136, 48
	v_readlane_b32 s6, v136, 0
	v_readlane_b32 s7, v136, 32
	v_mov_b32_e32 v136, s8
	v_mov_b32_e32 v137, s9
	v_pk_add_f32 v[136:137], s[6:7], v[136:137]
	s_ashr_i32 s19, s18, 31
	v_add_f32_e32 v136, v136, v137
	v_fmamk_f32 v136, v136, 0x3a000000, v206
	v_mul_f32_e32 v137, 0x4f800000, v136
	v_cmp_gt_f32_e64 s[6:7], s49, v136
	s_waitcnt vmcnt(11)
	v_pk_add_f32 v[96:97], v[96:97], 1.0 op_sel_hi:[1,0]
	v_cndmask_b32_e64 v136, v136, v137, s[6:7]
	v_sqrt_f32_e32 v137, v136
	s_nop 0
	v_add_u32_e32 v155, -1, v137
	v_fma_f32 v166, -v155, v137, v136
	v_cmp_ge_f32_e64 s[8:9], 0, v166
	v_add_u32_e32 v166, 1, v137
	s_nop 0
	v_cndmask_b32_e64 v155, v137, v155, s[8:9]
	v_fma_f32 v137, -v166, v137, v136
	v_cmp_lt_f32_e64 s[8:9], 0, v137
	s_nop 1
	v_cndmask_b32_e64 v137, v155, v166, s[8:9]
	v_mul_f32_e32 v155, 0x37800000, v137
	v_cndmask_b32_e64 v137, v137, v155, s[6:7]
	v_cmp_class_f32_e64 s[6:7], v136, v207
	v_div_fixup_f32 v166, v154, v160, 1.0
	v_pk_mul_f32 v[146:147], v[146:147], v[166:167] op_sel_hi:[1,0]
	v_cndmask_b32_e64 v136, v137, v136, s[6:7]
	v_div_scale_f32 v137, s[6:7], v136, v136, 1.0
	v_rcp_f32_e32 v155, v137
	s_waitcnt vmcnt(10)
	v_pk_mul_f32 v[146:147], v[100:101], v[146:147]
	v_pk_mul_f32 v[152:153], v[152:153], v[166:167] op_sel_hi:[1,0]
	v_pk_mul_f32 v[164:165], v[164:165], v[166:167] op_sel_hi:[1,0]
	v_fma_f32 v154, -v137, v155, 1.0
	v_fmac_f32_e32 v155, v154, v155
	v_div_scale_f32 v154, vcc, 1.0, v136, 1.0
	v_mul_f32_e32 v160, v154, v155
	v_fma_f32 v228, -v137, v160, v154
	v_fmac_f32_e32 v160, v228, v155
	v_fma_f32 v137, -v137, v160, v154
	v_div_fmas_f32 v137, v137, v155, v160
	v_div_fixup_f32 v160, v137, v136, 1.0
	v_lshlrev_b32_e32 v136, 3, v189
	v_and_b32_e32 v228, 8, v136
	v_pk_add_f32 v[136:137], v[98:99], 1.0 op_sel_hi:[1,0]
	s_waitcnt vmcnt(9)
	v_pk_fma_f32 v[154:155], v[96:97], v[146:147], v[104:105]
	v_pk_mul_f32 v[152:153], v[102:103], v[152:153]
	v_cvt_pk_bf16_f32 v146, v154, v155
	v_pk_mul_f32 v[170:171], v[170:171], v[160:161] op_sel_hi:[1,0]
	v_lshlrev_b32_e32 v186, 16, v146
	v_and_b32_e32 v187, 0xffff0000, v146
	v_sub_f32_e32 v186, v154, v186
	v_sub_f32_e32 v187, v155, v187
	v_pk_fma_f32 v[152:153], v[136:137], v[152:153], v[106:107]
	v_pk_mul_f32 v[170:171], v[100:101], v[170:171]
	v_cvt_pk_bf16_f32 v147, v152, v153
	v_cvt_pk_bf16_f32 v186, v186, v187
	v_pk_mul_f32 v[162:163], v[162:163], v[166:167] op_sel_hi:[1,0]
	v_lshlrev_b32_e32 v187, 16, v147
	v_and_b32_e32 v238, 0xffff0000, v147
	v_sub_f32_e32 v187, v152, v187
	v_sub_f32_e32 v238, v153, v238
	v_cvt_pk_bf16_f32 v187, v187, v238
	v_xor_b32_e32 v238, s43, v229
	v_lshlrev_b32_e32 v238, 4, v238
	v_add3_u32 v238, s44, v238, v228
	ds_write_b64 v238, v[146:147]
	v_add_u32_e32 v146, 0x10000, v238
	ds_write_b64 v146, v[186:187]
	v_pk_mul_f32 v[146:147], v[174:175], v[160:161] op_sel_hi:[1,0]
	v_xor_b32_e32 v238, s45, v229
	v_pk_mul_f32 v[146:147], v[102:103], v[146:147]
	v_lshlrev_b32_e32 v238, 4, v238
	v_pk_fma_f32 v[136:137], v[136:137], v[146:147], v[106:107]
	v_pk_fma_f32 v[146:147], v[96:97], v[170:171], v[104:105]
	v_lshlrev_b64 v[234:235], 2, v[76:77]
	v_cvt_pk_bf16_f32 v170, v146, v147
	v_cvt_pk_bf16_f32 v171, v136, v137
	v_lshl_add_u64 v[230:231], s[24:25], 0, v[234:235]
	v_lshlrev_b32_e32 v174, 16, v170
	v_and_b32_e32 v175, 0xffff0000, v170
	v_sub_f32_e32 v174, v146, v174
	v_sub_f32_e32 v175, v147, v175
	v_cvt_pk_bf16_f32 v174, v174, v175
	v_lshlrev_b32_e32 v175, 16, v171
	v_and_b32_e32 v184, 0xffff0000, v171
	v_sub_f32_e32 v175, v136, v175
	v_sub_f32_e32 v184, v137, v184
	v_cvt_pk_bf16_f32 v175, v175, v184
	v_lshl_add_u64 v[184:185], s[12:13], 0, v[234:235]
	global_load_dwordx4 v[96:99], v251, s[12:13]
	global_load_dwordx4 v[100:103], v251, s[24:25]
	global_load_dwordx4 v[104:107], v251, s[10:11]
	v_lshl_add_u64 v[234:235], s[10:11], 0, v[234:235]
	v_add3_u32 v238, s46, v238, v228
	ds_write_b64 v238, v[170:171]
	v_add_u32_e32 v170, 0x10000, v238
	ds_write_b64 v170, v[174:175]
	v_add_u32_e32 v238, 32, v229
	s_lshl_b64 s[6:7], s[18:19], 11
	s_add_u32 s6, s41, s6
	s_addc_u32 s7, s42, s7
	s_waitcnt vmcnt(11)
	v_pk_add_f32 v[110:111], v[110:111], 1.0 op_sel_hi:[1,0]
	v_pk_add_f32 v[108:109], v[108:109], 1.0 op_sel_hi:[1,0]
	s_waitcnt vmcnt(10)
	v_pk_mul_f32 v[162:163], v[162:163], v[112:113]
	v_pk_mul_f32 v[164:165], v[164:165], v[114:115]
	s_waitcnt vmcnt(9)
	v_pk_fma_f32 v[174:175], v[162:163], v[108:109], v[116:117]
	v_pk_fma_f32 v[170:171], v[164:165], v[110:111], v[118:119]
	v_cvt_pk_bf16_f32 v162, v174, v175
	s_nop 0
	v_lshlrev_b32_e32 v164, 16, v162
	v_and_b32_e32 v165, 0xffff0000, v162
	v_sub_f32_e32 v164, v174, v164
	v_sub_f32_e32 v165, v175, v165
	v_cvt_pk_bf16_f32 v163, v170, v171
	v_cvt_pk_bf16_f32 v164, v164, v165
	s_nop 0
	v_lshlrev_b32_e32 v165, 16, v163
	v_and_b32_e32 v239, 0xffff0000, v163
	v_sub_f32_e32 v165, v170, v165
	v_sub_f32_e32 v239, v171, v239
	v_cvt_pk_bf16_f32 v165, v165, v239
	v_xor_b32_e32 v239, s43, v238
	v_lshlrev_b32_e32 v239, 4, v239
	v_add3_u32 v239, s44, v239, v228
	ds_write_b64 v239, v[162:163]
	v_add_u32_e32 v162, 0x10000, v239
	ds_write_b64 v162, v[164:165]
	v_pk_mul_f32 v[164:165], v[180:181], v[160:161] op_sel_hi:[1,0]
	v_pk_mul_f32 v[162:163], v[182:183], v[160:161] op_sel_hi:[1,0]
	v_pk_mul_f32 v[164:165], v[164:165], v[112:113]
	v_pk_mul_f32 v[162:163], v[162:163], v[114:115]
	v_pk_fma_f32 v[164:165], v[164:165], v[108:109], v[116:117]
	v_pk_fma_f32 v[162:163], v[162:163], v[110:111], v[118:119]
	v_cvt_pk_bf16_f32 v184, v164, v165
	v_lshlrev_b64 v[234:235], 2, v[74:75]
	v_lshlrev_b32_e32 v180, 16, v184
	v_and_b32_e32 v181, 0xffff0000, v184
	v_sub_f32_e32 v180, v164, v180
	v_sub_f32_e32 v181, v165, v181
	v_cvt_pk_bf16_f32 v185, v162, v163
	v_cvt_pk_bf16_f32 v186, v180, v181
	v_lshl_add_u64 v[230:231], s[24:25], 0, v[234:235]
	v_lshlrev_b32_e32 v180, 16, v185
	v_and_b32_e32 v181, 0xffff0000, v185
	v_sub_f32_e32 v180, v162, v180
	v_sub_f32_e32 v181, v163, v181
	v_cvt_pk_bf16_f32 v187, v180, v181
	v_lshl_add_u64 v[180:181], s[12:13], 0, v[234:235]
	global_load_dwordx4 v[108:111], v251, s[12:13] offset:1024
	global_load_dwordx4 v[112:115], v251, s[24:25] offset:1024
	global_load_dwordx4 v[116:119], v251, s[10:11] offset:1024
	v_lshl_add_u64 v[234:235], s[10:11], 0, v[234:235]
	v_xor_b32_e32 v238, s45, v238
	v_lshlrev_b32_e32 v238, 4, v238
	v_add3_u32 v238, s46, v238, v228
	ds_write_b64 v238, v[184:185]
	v_add_u32_e32 v184, 0x10000, v238
	ds_write_b64 v184, v[186:187]
	v_mov_b32_e32 v184, v148
	v_mov_b32_e32 v185, v150
	v_pk_mul_f32 v[184:185], v[184:185], v[166:167] op_sel_hi:[1,0]
	s_waitcnt vmcnt(11)
	v_pk_add_f32 v[238:239], v[120:121], 1.0 op_sel_hi:[1,0]
	v_mov_b32_e32 v180, v156
	v_mov_b32_e32 v181, v158
	v_pk_mul_f32 v[180:181], v[180:181], v[166:167] op_sel_hi:[1,0]
	v_pk_add_f32 v[122:123], v[122:123], 1.0 op_sel_hi:[1,0]
	s_waitcnt vmcnt(10)
	v_pk_mul_f32 v[186:187], v[184:185], v[124:125]
	v_pk_mul_f32 v[180:181], v[180:181], v[126:127]
	s_waitcnt vmcnt(9)
	v_pk_fma_f32 v[186:187], v[186:187], v[238:239], v[212:213]
	v_pk_fma_f32 v[184:185], v[180:181], v[122:123], v[214:215]
	v_cvt_pk_bf16_f32 v180, v186, v187
	v_mov_b32_e32 v158, v157
	v_lshlrev_b32_e32 v148, 16, v180
	v_sub_f32_e32 v148, v186, v148
	v_and_b32_e32 v150, 0xffff0000, v180
	v_cvt_pk_bf16_f32 v181, v184, v185
	v_sub_f32_e32 v150, v187, v150
	v_cvt_pk_bf16_f32 v240, v148, v150
	v_lshlrev_b32_e32 v148, 16, v181
	v_sub_f32_e32 v148, v184, v148
	v_and_b32_e32 v150, 0xffff0000, v181
	v_sub_f32_e32 v150, v185, v150
	v_cvt_pk_bf16_f32 v241, v148, v150
	v_xor_b32_e32 v148, s43, v246
	v_lshlrev_b32_e32 v148, 4, v148
	v_add3_u32 v148, s44, v148, v228
	ds_write_b64 v148, v[180:181]
	v_add_u32_e32 v148, 0x10000, v148
	ds_write_b64 v148, v[240:241]
	v_mov_b32_e32 v180, v176
	v_mov_b32_e32 v181, v178
	v_mov_b32_e32 v240, v168
	v_mov_b32_e32 v241, v172
	v_pk_mul_f32 v[180:181], v[180:181], v[160:161] op_sel_hi:[1,0]
	v_pk_mul_f32 v[240:241], v[240:241], v[160:161] op_sel_hi:[1,0]
	v_pk_mul_f32 v[180:181], v[180:181], v[126:127]
	v_pk_mul_f32 v[124:125], v[240:241], v[124:125]
	v_pk_fma_f32 v[180:181], v[180:181], v[122:123], v[214:215]
	v_pk_fma_f32 v[182:183], v[124:125], v[238:239], v[212:213]
	v_lshlrev_b64 v[238:239], 2, v[72:73]
	v_cvt_pk_bf16_f32 v242, v182, v183
	v_cvt_pk_bf16_f32 v243, v180, v181
	v_lshl_add_u64 v[230:231], s[12:13], 0, v[238:239]
	v_lshlrev_b32_e32 v148, 16, v242
	v_and_b32_e32 v150, 0xffff0000, v242
	v_sub_f32_e32 v148, v182, v148
	v_sub_f32_e32 v150, v183, v150
	v_cvt_pk_bf16_f32 v244, v148, v150
	v_lshlrev_b32_e32 v148, 16, v243
	v_and_b32_e32 v150, 0xffff0000, v243
	v_lshl_add_u64 v[234:235], s[24:25], 0, v[238:239]
	v_sub_f32_e32 v148, v180, v148
	v_sub_f32_e32 v150, v181, v150
	v_cvt_pk_bf16_f32 v245, v148, v150
	global_load_dwordx4 v[120:123], v251, s[12:13] offset:2048
	global_load_dwordx4 v[124:127], v251, s[24:25] offset:2048
	global_load_dwordx4 v[212:215], v251, s[10:11] offset:2048
	v_lshl_add_u64 v[238:239], s[10:11], 0, v[238:239]
	v_xor_b32_e32 v148, s45, v246
	v_lshlrev_b32_e32 v148, 4, v148
	v_add3_u32 v148, s46, v148, v228
	ds_write_b64 v148, v[242:243]
	v_add_u32_e32 v148, 0x10000, v148
	v_mov_b32_e32 v150, v149
	ds_write_b64 v148, v[244:245]
	v_pk_mul_f32 v[156:157], v[158:159], v[166:167] op_sel_hi:[1,0]
	v_pk_mul_f32 v[148:149], v[150:151], v[166:167] op_sel_hi:[1,0]
	v_add_u32_e32 v242, 0x60, v229
	v_mov_b32_e32 v172, v169
	v_mov_b32_e32 v178, v177
	v_add_u32_e32 v246, 0x80, v229
	s_waitcnt vmcnt(11)
	v_pk_add_f32 v[218:219], v[218:219], 1.0 op_sel_hi:[1,0]
	v_pk_add_f32 v[216:217], v[216:217], 1.0 op_sel_hi:[1,0]
	s_waitcnt vmcnt(10)
	v_pk_mul_f32 v[148:149], v[148:149], v[220:221]
	v_pk_mul_f32 v[150:151], v[156:157], v[222:223]
	s_waitcnt vmcnt(9)
	v_pk_fma_f32 v[158:159], v[148:149], v[216:217], v[224:225]
	v_pk_fma_f32 v[156:157], v[150:151], v[218:219], v[226:227]
	v_cvt_pk_bf16_f32 v148, v158, v159
	s_nop 0
	v_lshlrev_b32_e32 v150, 16, v148
	v_and_b32_e32 v151, 0xffff0000, v148
	v_sub_f32_e32 v150, v158, v150
	v_sub_f32_e32 v151, v159, v151
	v_cvt_pk_bf16_f32 v149, v156, v157
	v_cvt_pk_bf16_f32 v150, v150, v151
	s_nop 0
	v_lshlrev_b32_e32 v151, 16, v149
	v_and_b32_e32 v168, 0xffff0000, v149
	v_sub_f32_e32 v151, v156, v151
	v_sub_f32_e32 v168, v157, v168
	v_cvt_pk_bf16_f32 v151, v151, v168
	v_xor_b32_e32 v168, s43, v242
	v_lshlrev_b32_e32 v168, 4, v168
	v_add3_u32 v168, s44, v168, v228
	ds_write_b64 v168, v[148:149]
	v_add_u32_e32 v148, 0x10000, v168
	ds_write_b64 v148, v[150:151]
	v_pk_mul_f32 v[150:151], v[172:173], v[160:161] op_sel_hi:[1,0]
	v_pk_mul_f32 v[148:149], v[178:179], v[160:161] op_sel_hi:[1,0]
	v_pk_mul_f32 v[150:151], v[150:151], v[220:221]
	v_pk_mul_f32 v[148:149], v[148:149], v[222:223]
	v_pk_fma_f32 v[150:151], v[150:151], v[216:217], v[224:225]
	v_pk_fma_f32 v[148:149], v[148:149], v[218:219], v[226:227]
	v_cvt_pk_bf16_f32 v168, v150, v151
	v_lshlrev_b64 v[234:235], 2, v[70:71]
	v_lshlrev_b32_e32 v172, 16, v168
	v_and_b32_e32 v173, 0xffff0000, v168
	v_sub_f32_e32 v172, v150, v172
	v_sub_f32_e32 v173, v151, v173
	v_cvt_pk_bf16_f32 v169, v148, v149
	v_cvt_pk_bf16_f32 v172, v172, v173
	v_lshl_add_u64 v[230:231], s[24:25], 0, v[234:235]
	v_lshlrev_b32_e32 v173, 16, v169
	v_and_b32_e32 v176, 0xffff0000, v169
	v_sub_f32_e32 v173, v148, v173
	v_sub_f32_e32 v176, v149, v176
	v_cvt_pk_bf16_f32 v173, v173, v176
	v_lshl_add_u64 v[176:177], s[12:13], 0, v[234:235]
	global_load_dwordx4 v[216:219], v251, s[12:13] offset:3072
	global_load_dwordx4 v[220:223], v251, s[24:25] offset:3072
	global_load_dwordx4 v[224:227], v251, s[10:11] offset:3072
	v_lshl_add_u64 v[234:235], s[10:11], 0, v[234:235]
	v_xor_b32_e32 v238, s45, v242
	v_lshlrev_b32_e32 v238, 4, v238
	v_add3_u32 v238, s46, v238, v228
	ds_write_b64 v238, v[168:169]
	v_add_u32_e32 v168, 0x10000, v238
	ds_write_b64 v168, v[172:173]
	s_waitcnt vmcnt(11)
	v_pk_add_f32 v[168:169], v[98:99], 1.0 op_sel_hi:[1,0]
	v_mov_b32_e32 v178, v92
	v_mov_b32_e32 v179, v94
	v_pk_mul_f32 v[178:179], v[178:179], v[166:167] op_sel_hi:[1,0]
	v_pk_add_f32 v[172:173], v[96:97], 1.0 op_sel_hi:[1,0]
	v_mov_b32_e32 v176, v130
	v_mov_b32_e32 v177, v134
	s_waitcnt vmcnt(10)
	v_pk_mul_f32 v[178:179], v[178:179], v[100:101]
	v_pk_mul_f32 v[176:177], v[176:177], v[166:167] op_sel_hi:[1,0]
	s_waitcnt vmcnt(9)
	v_pk_fma_f32 v[178:179], v[178:179], v[172:173], v[104:105]
	v_pk_mul_f32 v[176:177], v[176:177], v[102:103]
	v_cvt_pk_bf16_f32 v238, v178, v179
	v_mov_b32_e32 v134, v131
	v_lshlrev_b32_e32 v92, 16, v238
	v_sub_f32_e32 v92, v178, v92
	v_and_b32_e32 v94, 0xffff0000, v238
	v_pk_fma_f32 v[176:177], v[176:177], v[168:169], v[106:107]
	v_sub_f32_e32 v94, v179, v94
	v_cvt_pk_bf16_f32 v239, v176, v177
	v_cvt_pk_bf16_f32 v240, v92, v94
	v_pk_mul_f32 v[130:131], v[134:135], v[166:167] op_sel_hi:[1,0]
	v_lshlrev_b32_e32 v92, 16, v239
	v_sub_f32_e32 v92, v176, v92
	v_and_b32_e32 v94, 0xffff0000, v239
	v_sub_f32_e32 v94, v177, v94
	v_cvt_pk_bf16_f32 v241, v92, v94
	v_xor_b32_e32 v92, s43, v246
	v_lshlrev_b32_e32 v92, 4, v92
	v_add3_u32 v92, s44, v92, v228
	ds_write_b64 v92, v[238:239]
	v_add_u32_e32 v92, 0x10000, v92
	ds_write_b64 v92, v[240:241]
	v_mov_b32_e32 v240, v138
	v_mov_b32_e32 v241, v140
	v_pk_mul_f32 v[240:241], v[240:241], v[160:161] op_sel_hi:[1,0]
	v_mov_b32_e32 v238, v142
	v_mov_b32_e32 v239, v144
	v_pk_mul_f32 v[100:101], v[240:241], v[100:101]
	v_pk_mul_f32 v[238:239], v[238:239], v[160:161] op_sel_hi:[1,0]
	v_pk_fma_f32 v[172:173], v[100:101], v[172:173], v[104:105]
	v_pk_mul_f32 v[102:103], v[238:239], v[102:103]
	v_cvt_pk_bf16_f32 v242, v172, v173
	v_lshlrev_b64 v[238:239], 2, v[68:69]
	v_lshlrev_b32_e32 v92, 16, v242
	v_and_b32_e32 v94, 0xffff0000, v242
	v_sub_f32_e32 v92, v172, v92
	v_sub_f32_e32 v94, v173, v94
	v_pk_fma_f32 v[168:169], v[102:103], v[168:169], v[106:107]
	v_lshl_add_u64 v[230:231], s[12:13], 0, v[238:239]
	v_cvt_pk_bf16_f32 v243, v168, v169
	v_cvt_pk_bf16_f32 v244, v92, v94
	v_lshl_add_u64 v[234:235], s[24:25], 0, v[238:239]
	v_lshlrev_b32_e32 v92, 16, v243
	v_and_b32_e32 v94, 0xffff0000, v243
	v_sub_f32_e32 v92, v168, v92
	v_sub_f32_e32 v94, v169, v94
	v_cvt_pk_bf16_f32 v245, v92, v94
	v_lshl_add_u64 v[238:239], s[10:11], 0, v[238:239]
	v_xor_b32_e32 v92, s45, v246
	v_lshlrev_b32_e32 v92, 4, v92
	v_add3_u32 v92, s46, v92, v228
	ds_write_b64 v92, v[242:243]
	v_add_u32_e32 v92, 0x10000, v92
	v_mov_b32_e32 v94, v93
	ds_write_b64 v92, v[244:245]
	v_pk_mul_f32 v[92:93], v[94:95], v[166:167] op_sel_hi:[1,0]
	v_add_u32_e32 v242, 0xa0, v229
	v_mov_b32_e32 v140, v139
	v_mov_b32_e32 v144, v143
	v_add_u32_e32 v246, 0xc0, v229
	s_waitcnt vmcnt(8)
	v_pk_add_f32 v[110:111], v[110:111], 1.0 op_sel_hi:[1,0]
	v_pk_add_f32 v[108:109], v[108:109], 1.0 op_sel_hi:[1,0]
	s_waitcnt vmcnt(7)
	v_pk_mul_f32 v[92:93], v[92:93], v[112:113]
	v_pk_mul_f32 v[94:95], v[130:131], v[114:115]
	s_waitcnt vmcnt(6)
	v_pk_fma_f32 v[134:135], v[92:93], v[108:109], v[116:117]
	v_pk_fma_f32 v[130:131], v[94:95], v[110:111], v[118:119]
	v_cvt_pk_bf16_f32 v92, v134, v135
	s_nop 0
	v_lshlrev_b32_e32 v94, 16, v92
	v_and_b32_e32 v95, 0xffff0000, v92
	v_sub_f32_e32 v94, v134, v94
	v_sub_f32_e32 v95, v135, v95
	v_cvt_pk_bf16_f32 v93, v130, v131
	v_cvt_pk_bf16_f32 v94, v94, v95
	s_nop 0
	v_lshlrev_b32_e32 v95, 16, v93
	v_and_b32_e32 v138, 0xffff0000, v93
	v_sub_f32_e32 v95, v130, v95
	v_sub_f32_e32 v138, v131, v138
	v_cvt_pk_bf16_f32 v95, v95, v138
	v_xor_b32_e32 v138, s43, v242
	v_lshlrev_b32_e32 v138, 4, v138
	v_add3_u32 v138, s44, v138, v228
	ds_write_b64 v138, v[92:93]
	v_add_u32_e32 v92, 0x10000, v138
	ds_write_b64 v92, v[94:95]
	v_pk_mul_f32 v[94:95], v[140:141], v[160:161] op_sel_hi:[1,0]
	v_pk_mul_f32 v[92:93], v[144:145], v[160:161] op_sel_hi:[1,0]
	v_pk_mul_f32 v[94:95], v[94:95], v[112:113]
	v_pk_mul_f32 v[92:93], v[92:93], v[114:115]
	v_pk_fma_f32 v[94:95], v[94:95], v[108:109], v[116:117]
	v_pk_fma_f32 v[92:93], v[92:93], v[110:111], v[118:119]
	v_cvt_pk_bf16_f32 v234, v94, v95
	v_lshlrev_b64 v[230:231], 2, v[66:67]
	v_lshlrev_b32_e32 v138, 16, v234
	v_and_b32_e32 v139, 0xffff0000, v234
	v_sub_f32_e32 v138, v94, v138
	v_sub_f32_e32 v139, v95, v139
	v_cvt_pk_bf16_f32 v235, v92, v93
	v_cvt_pk_bf16_f32 v236, v138, v139
	v_lshl_add_u64 v[142:143], s[24:25], 0, v[230:231]
	v_lshlrev_b32_e32 v138, 16, v235
	v_and_b32_e32 v139, 0xffff0000, v235
	v_sub_f32_e32 v138, v92, v138
	v_sub_f32_e32 v139, v93, v139
	v_cvt_pk_bf16_f32 v237, v138, v139
	v_lshl_add_u64 v[138:139], s[12:13], 0, v[230:231]
	v_lshl_add_u64 v[230:231], s[10:11], 0, v[230:231]
	v_xor_b32_e32 v238, s45, v242
	v_lshlrev_b32_e32 v238, 4, v238
	v_add3_u32 v238, s46, v238, v228
	ds_write_b64 v238, v[234:235]
	v_add_u32_e32 v234, 0x10000, v238
	ds_write_b64 v234, v[236:237]
	v_mov_b32_e32 v236, v80
	v_mov_b32_e32 v237, v82
	v_pk_mul_f32 v[236:237], v[236:237], v[166:167] op_sel_hi:[1,0]
	s_waitcnt vmcnt(5)
	v_pk_add_f32 v[234:235], v[120:121], 1.0 op_sel_hi:[1,0]
	v_mov_b32_e32 v138, v84
	v_mov_b32_e32 v139, v86
	v_pk_mul_f32 v[138:139], v[138:139], v[166:167] op_sel_hi:[1,0]
	v_pk_add_f32 v[122:123], v[122:123], 1.0 op_sel_hi:[1,0]
	s_waitcnt vmcnt(4)
	v_pk_mul_f32 v[236:237], v[236:237], v[124:125]
	v_pk_mul_f32 v[138:139], v[138:139], v[126:127]
	s_waitcnt vmcnt(3)
	v_pk_fma_f32 v[240:241], v[236:237], v[234:235], v[212:213]
	v_pk_fma_f32 v[238:239], v[138:139], v[122:123], v[214:215]
	v_cvt_pk_bf16_f32 v138, v240, v241
	v_mov_b32_e32 v86, v85
	v_lshlrev_b32_e32 v80, 16, v138
	v_sub_f32_e32 v80, v240, v80
	v_and_b32_e32 v82, 0xffff0000, v138
	v_cvt_pk_bf16_f32 v139, v238, v239
	v_sub_f32_e32 v82, v241, v82
	v_cvt_pk_bf16_f32 v236, v80, v82
	v_lshlrev_b32_e32 v80, 16, v139
	v_sub_f32_e32 v80, v238, v80
	v_and_b32_e32 v82, 0xffff0000, v139
	v_sub_f32_e32 v82, v239, v82
	v_cvt_pk_bf16_f32 v237, v80, v82
	v_xor_b32_e32 v80, s43, v246
	v_lshlrev_b32_e32 v80, 4, v80
	v_add3_u32 v80, s44, v80, v228
	ds_write_b64 v80, v[138:139]
	v_add_u32_e32 v80, 0x10000, v80
	ds_write_b64 v80, v[236:237]
	v_mov_b32_e32 v138, v128
	v_mov_b32_e32 v139, v132
	v_mov_b32_e32 v236, v88
	v_mov_b32_e32 v237, v90
	v_pk_mul_f32 v[138:139], v[138:139], v[160:161] op_sel_hi:[1,0]
	v_pk_mul_f32 v[236:237], v[236:237], v[160:161] op_sel_hi:[1,0]
	v_pk_mul_f32 v[138:139], v[138:139], v[126:127]
	v_pk_mul_f32 v[124:125], v[236:237], v[124:125]
	v_pk_fma_f32 v[138:139], v[138:139], v[122:123], v[214:215]
	v_pk_fma_f32 v[140:141], v[124:125], v[234:235], v[212:213]
	v_lshlrev_b64 v[234:235], 2, v[64:65]
	v_cvt_pk_bf16_f32 v242, v140, v141
	v_cvt_pk_bf16_f32 v243, v138, v139
	v_lshl_add_u64 v[142:143], s[12:13], 0, v[234:235]
	v_lshlrev_b32_e32 v80, 16, v242
	v_and_b32_e32 v82, 0xffff0000, v242
	v_sub_f32_e32 v80, v140, v80
	v_sub_f32_e32 v82, v141, v82
	v_cvt_pk_bf16_f32 v244, v80, v82
	v_lshlrev_b32_e32 v80, 16, v243
	v_and_b32_e32 v82, 0xffff0000, v243
	v_lshl_add_u64 v[230:231], s[24:25], 0, v[234:235]
	v_sub_f32_e32 v80, v138, v80
	v_sub_f32_e32 v82, v139, v82
	v_cvt_pk_bf16_f32 v245, v80, v82
	v_lshl_add_u64 v[234:235], s[10:11], 0, v[234:235]
	v_xor_b32_e32 v80, s45, v246
	v_lshlrev_b32_e32 v80, 4, v80
	v_add3_u32 v80, s46, v80, v228
	ds_write_b64 v80, v[242:243]
	v_add_u32_e32 v80, 0x10000, v80
	v_mov_b32_e32 v82, v81
	ds_write_b64 v80, v[244:245]
	v_pk_mul_f32 v[80:81], v[82:83], v[166:167] op_sel_hi:[1,0]
	v_pk_mul_f32 v[84:85], v[86:87], v[166:167] op_sel_hi:[1,0]
	v_add_u32_e32 v128, 0xe0, v229
	v_mov_b32_e32 v90, v89
	v_mov_b32_e32 v132, v129
	s_waitcnt vmcnt(2)
	v_pk_add_f32 v[216:217], v[216:217], 1.0 op_sel_hi:[1,0]
	v_pk_add_f32 v[218:219], v[218:219], 1.0 op_sel_hi:[1,0]
	s_waitcnt vmcnt(1)
	v_pk_mul_f32 v[80:81], v[80:81], v[220:221]
	v_pk_mul_f32 v[82:83], v[84:85], v[222:223]
	s_waitcnt vmcnt(0)
	v_pk_fma_f32 v[80:81], v[80:81], v[216:217], v[224:225]
	v_pk_fma_f32 v[82:83], v[82:83], v[218:219], v[226:227]
	v_cvt_pk_bf16_f32 v84, v80, v81
	s_nop 0
	v_lshlrev_b32_e32 v86, 16, v84
	v_and_b32_e32 v87, 0xffff0000, v84
	v_sub_f32_e32 v86, v80, v86
	v_sub_f32_e32 v87, v81, v87
	v_cvt_pk_bf16_f32 v85, v82, v83
	v_cvt_pk_bf16_f32 v86, v86, v87
	s_nop 0
	v_lshlrev_b32_e32 v87, 16, v85
	v_and_b32_e32 v88, 0xffff0000, v85
	v_sub_f32_e32 v87, v82, v87
	v_sub_f32_e32 v88, v83, v88
	v_cvt_pk_bf16_f32 v87, v87, v88
	v_xor_b32_e32 v88, s43, v128
	v_lshlrev_b32_e32 v88, 4, v88
	v_add3_u32 v88, s44, v88, v228
	ds_write_b64 v88, v[84:85]
	v_add_u32_e32 v84, 0x10000, v88
	ds_write_b64 v84, v[86:87]
	v_pk_mul_f32 v[86:87], v[90:91], v[160:161] op_sel_hi:[1,0]
	v_pk_mul_f32 v[84:85], v[132:133], v[160:161] op_sel_hi:[1,0]
	v_pk_mul_f32 v[86:87], v[86:87], v[220:221]
	v_pk_mul_f32 v[84:85], v[84:85], v[222:223]
	v_pk_fma_f32 v[86:87], v[86:87], v[216:217], v[224:225]
	v_xor_b32_e32 v128, s45, v128
	v_cvt_pk_bf16_f32 v88, v86, v87
	v_pk_fma_f32 v[84:85], v[84:85], v[218:219], v[226:227]
	s_cmp_lt_i32 s56, s39
	s_cbranch_scc0 .Lpf_skip_0
	s_add_i32 s98, s38, s18
	s_ashr_i32 s99, s98, 31
	s_lshl_b64 s[100:101], s[98:99], 11
	s_lshl_b64 s[98:99], s[98:99], 12
	s_add_u32 s98, s35, s98
	s_addc_u32 s99, s36, s99
	s_add_u32 s100, s37, s100
	v_lshlrev_b64 v[112:113], 1, v[78:79]
	s_addc_u32 s101, s40, s101
	v_lshl_add_u64 v[110:111], s[98:99], 0, v[112:113]
	s_add_i32 s98, s47, s18
	s_ashr_i32 s99, s98, 31
	v_lshl_add_u64 v[114:115], s[100:101], 0, v[78:79]
	s_lshl_b64 s[100:101], s[98:99], 11
	s_lshl_b64 s[98:99], s[98:99], 12
	s_add_u32 s98, s35, s98
	s_addc_u32 s99, s36, s99
	s_add_u32 s100, s37, s100
	s_addc_u32 s101, s40, s101
	v_lshl_add_u64 v[126:127], s[98:99], 0, v[112:113]
	global_load_dwordx2 v[96:97], v[110:111], off
	global_load_dwordx2 v[98:99], v[110:111], off offset:512
	global_load_dwordx2 v[100:101], v[110:111], off offset:1024
	global_load_dwordx2 v[102:103], v[110:111], off offset:1536
	global_load_dwordx2 v[104:105], v[110:111], off offset:2048
	global_load_dwordx2 v[106:107], v[110:111], off offset:2560
	global_load_dwordx2 v[108:109], v[110:111], off offset:3072
	s_nop 0
	global_load_dwordx2 v[110:111], v[110:111], off offset:3584
	s_nop 0
	global_load_dword v212, v[114:115], off
	global_load_dword v213, v[114:115], off offset:256
	global_load_dword v214, v[114:115], off offset:512
	global_load_dword v215, v[114:115], off offset:768
	global_load_dword v216, v[114:115], off offset:1024
	global_load_dword v217, v[114:115], off offset:1280
	global_load_dword v218, v[114:115], off offset:1536
	global_load_dword v219, v[114:115], off offset:1792
	v_lshl_add_u64 v[250:251], s[100:101], 0, v[78:79]
	global_load_dwordx2 v[112:113], v[126:127], off
	global_load_dwordx2 v[114:115], v[126:127], off offset:512
	global_load_dwordx2 v[116:117], v[126:127], off offset:1024
	global_load_dwordx2 v[118:119], v[126:127], off offset:1536
	global_load_dwordx2 v[120:121], v[126:127], off offset:2048
	global_load_dwordx2 v[122:123], v[126:127], off offset:2560
	global_load_dwordx2 v[124:125], v[126:127], off offset:3072
	s_nop 0
	global_load_dwordx2 v[126:127], v[126:127], off offset:3584
	s_nop 0
	global_load_dword v220, v[250:251], off
	global_load_dword v221, v[250:251], off offset:256
	global_load_dword v222, v[250:251], off offset:512
	global_load_dword v223, v[250:251], off offset:768
	global_load_dword v224, v[250:251], off offset:1024
	global_load_dword v225, v[250:251], off offset:1280
	global_load_dword v226, v[250:251], off offset:1536
	global_load_dword v227, v[250:251], off offset:1792

.LBB0_5170:
	v_cvt_pk_f32_fp8_e32 v[152:153], v146
	v_cvt_pk_f32_fp8_sdwa v[156:157], v146 src0_sel:WORD_1
	v_lshlrev_b32_e32 v146, 16, v130
	v_and_b32_e32 v147, 0xffff0000, v130
	v_lshlrev_b32_e32 v130, 16, v131
	v_and_b32_e32 v131, 0xffff0000, v131
	v_pk_add_f32 v[146:147], v[152:153], v[146:147]
	v_pk_add_f32 v[152:153], v[156:157], v[130:131]
	v_cvt_pk_f32_fp8_e32 v[130:131], v150
	v_cvt_pk_f32_fp8_sdwa v[150:151], v150 src0_sel:WORD_1
	v_lshlrev_b32_e32 v156, 16, v94
	v_and_b32_e32 v157, 0xffff0000, v94
	v_lshlrev_b32_e32 v94, 16, v95
	v_and_b32_e32 v95, 0xffff0000, v95
	v_pk_add_f32 v[164:165], v[150:151], v[94:95]
	v_cvt_pk_f32_fp8_e32 v[94:95], v149
	v_cvt_pk_f32_fp8_e32 v[150:151], v148
	v_pk_add_f32 v[162:163], v[130:131], v[156:157]
	v_cvt_pk_f32_fp8_sdwa v[130:131], v149 src0_sel:WORD_1
	v_cvt_pk_f32_fp8_sdwa v[158:159], v148 src0_sel:WORD_1
	v_lshlrev_b32_e32 v149, 16, v92
	v_lshlrev_b32_e32 v148, 16, v84
	v_mov_b32_e32 v156, v94
	v_mov_b32_e32 v157, v150
	v_pk_add_f32 v[148:149], v[156:157], v[148:149]
	v_and_b32_e32 v157, 0xffff0000, v92
	v_and_b32_e32 v156, 0xffff0000, v84
	v_mov_b32_e32 v150, v95
	v_pk_add_f32 v[150:151], v[150:151], v[156:157]
	v_lshlrev_b32_e32 v95, 16, v93
	v_lshlrev_b32_e32 v94, 16, v85
	v_mov_b32_e32 v156, v130
	v_mov_b32_e32 v157, v158
	v_pk_add_f32 v[156:157], v[156:157], v[94:95]
	v_and_b32_e32 v92, 0xffff0000, v85
	v_cvt_pk_f32_fp8_e32 v[84:85], v135
	v_cvt_pk_f32_fp8_e32 v[94:95], v134
	v_cvt_pk_f32_fp8_sdwa v[174:175], v135 src0_sel:WORD_1
	v_cvt_pk_f32_fp8_sdwa v[134:135], v134 src0_sel:WORD_1
	v_and_b32_e32 v93, 0xffff0000, v93
	v_mov_b32_e32 v158, v131
	v_pk_add_f32 v[158:159], v[158:159], v[92:93]
	v_lshlrev_b32_e32 v93, 16, v82
	v_lshlrev_b32_e32 v92, 16, v80
	v_mov_b32_e32 v130, v84
	v_mov_b32_e32 v131, v94
	v_pk_add_f32 v[92:93], v[130:131], v[92:93]
	v_and_b32_e32 v131, 0xffff0000, v82
	v_and_b32_e32 v130, 0xffff0000, v80
	v_mov_b32_e32 v94, v85
	v_pk_add_f32 v[94:95], v[94:95], v[130:131]
	v_lshlrev_b32_e32 v85, 16, v83
	v_lshlrev_b32_e32 v84, 16, v81
	v_mov_b32_e32 v130, v174
	v_mov_b32_e32 v131, v134
	v_and_b32_e32 v83, 0xffff0000, v83
	v_and_b32_e32 v82, 0xffff0000, v81
	v_mov_b32_e32 v134, v175
	v_pk_add_f32 v[130:131], v[130:131], v[84:85]
	v_pk_add_f32 v[134:135], v[134:135], v[82:83]
	v_cvt_pk_f32_fp8_e32 v[82:83], v173
	v_cvt_pk_f32_fp8_e32 v[84:85], v171
	v_cvt_pk_f32_fp8_sdwa v[174:175], v173 src0_sel:WORD_1
	v_cvt_pk_f32_fp8_sdwa v[176:177], v171 src0_sel:WORD_1
	v_lshlrev_b32_e32 v81, 16, v144
	v_lshlrev_b32_e32 v80, 16, v86
	v_mov_b32_e32 v178, v82
	v_mov_b32_e32 v179, v84
	v_pk_add_f32 v[80:81], v[178:179], v[80:81]
	v_and_b32_e32 v179, 0xffff0000, v144
	v_and_b32_e32 v178, 0xffff0000, v86
	v_mov_b32_e32 v84, v83
	v_pk_add_f32 v[82:83], v[84:85], v[178:179]
	v_lshlrev_b32_e32 v85, 16, v145
	v_mov_b32_e32 v179, v176
	v_and_b32_e32 v145, 0xffff0000, v145
	v_and_b32_e32 v144, 0xffff0000, v87
	v_mov_b32_e32 v176, v175
	v_lshlrev_b32_e32 v84, 16, v87
	v_pk_add_f32 v[86:87], v[176:177], v[144:145]
	v_cvt_pk_f32_fp8_e32 v[144:145], v170
	v_mov_b32_e32 v178, v174
	v_cvt_pk_f32_fp8_sdwa v[174:175], v170 src0_sel:WORD_1
	v_lshlrev_b32_e32 v170, 16, v140
	v_and_b32_e32 v171, 0xffff0000, v140
	v_pk_add_f32 v[170:171], v[144:145], v[170:171]
	v_cvt_pk_f32_fp8_sdwa v[144:145], v172 src0_sel:WORD_1
	v_lshlrev_b32_e32 v140, 16, v141
	v_and_b32_e32 v141, 0xffff0000, v141
	v_pk_add_f32 v[174:175], v[174:175], v[140:141]
	v_cvt_pk_f32_fp8_e32 v[140:141], v172
	v_lshlrev_b32_e32 v172, 16, v138
	v_and_b32_e32 v173, 0xffff0000, v138
	v_lshlrev_b32_e32 v138, 16, v139
	v_and_b32_e32 v139, 0xffff0000, v139
	v_pk_add_f32 v[182:183], v[144:145], v[138:139]
	v_cvt_pk_f32_fp8_e32 v[138:139], v169
	v_cvt_pk_f32_fp8_e32 v[144:145], v168
	v_pk_add_f32 v[84:85], v[178:179], v[84:85]
	v_pk_add_f32 v[180:181], v[140:141], v[172:173]
	v_cvt_pk_f32_fp8_sdwa v[140:141], v169 src0_sel:WORD_1
	v_cvt_pk_f32_fp8_sdwa v[178:179], v168 src0_sel:WORD_1
	v_lshlrev_b32_e32 v169, 16, v136
	v_lshlrev_b32_e32 v168, 16, v128
	v_mov_b32_e32 v172, v138
	v_mov_b32_e32 v173, v144
	v_pk_add_f32 v[168:169], v[172:173], v[168:169]
	v_and_b32_e32 v173, 0xffff0000, v136
	v_and_b32_e32 v172, 0xffff0000, v128
	v_mov_b32_e32 v144, v139
	v_pk_add_f32 v[172:173], v[144:145], v[172:173]
	v_lshlrev_b32_e32 v139, 16, v137
	v_lshlrev_b32_e32 v138, 16, v129
	v_mov_b32_e32 v144, v140
	v_mov_b32_e32 v145, v178
	v_pk_add_f32 v[176:177], v[144:145], v[138:139]
	v_and_b32_e32 v136, 0xffff0000, v129
	v_cvt_pk_f32_fp8_e32 v[128:129], v166
	v_cvt_pk_f32_fp8_e32 v[138:139], v160
	v_cvt_pk_f32_fp8_sdwa v[144:145], v166 src0_sel:WORD_1
	v_cvt_pk_f32_fp8_sdwa v[184:185], v160 src0_sel:WORD_1
	v_and_b32_e32 v137, 0xffff0000, v137
	v_mov_b32_e32 v178, v141
	v_pk_add_f32 v[178:179], v[178:179], v[136:137]
	v_lshlrev_b32_e32 v137, 16, v90
	v_lshlrev_b32_e32 v136, 16, v88
	v_mov_b32_e32 v140, v128
	v_mov_b32_e32 v141, v138
	v_pk_add_f32 v[136:137], v[140:141], v[136:137]
	v_and_b32_e32 v141, 0xffff0000, v90
	v_and_b32_e32 v140, 0xffff0000, v88
	v_mov_b32_e32 v138, v129
	v_pk_add_f32 v[138:139], v[138:139], v[140:141]
	v_lshlrev_b32_e32 v129, 16, v91
	v_lshlrev_b32_e32 v128, 16, v89
	v_mov_b32_e32 v140, v144
	v_mov_b32_e32 v141, v184
	v_and_b32_e32 v91, 0xffff0000, v91
	v_and_b32_e32 v90, 0xffff0000, v89
	v_mov_b32_e32 v184, v145
	v_pk_add_f32 v[140:141], v[140:141], v[128:129]
	v_pk_add_f32 v[144:145], v[184:185], v[90:91]
	v_cvt_pk_f32_fp8_e32 v[90:91], v155
	v_cvt_pk_f32_fp8_e32 v[128:129], v154
	v_lshlrev_b32_e32 v89, 16, v142
	v_lshlrev_b32_e32 v88, 16, v132
	v_mov_b32_e32 v186, v90
	v_mov_b32_e32 v187, v128
	v_pk_mul_f32 v[228:229], v[146:147], v[146:147]
	v_pk_mul_f32 v[232:233], v[162:163], v[162:163]
	v_pk_add_f32 v[88:89], v[186:187], v[88:89]
	v_and_b32_e32 v187, 0xffff0000, v142
	v_and_b32_e32 v186, 0xffff0000, v132
	v_pk_mul_f32 v[230:231], v[152:153], v[152:153]
	v_pk_mul_f32 v[234:235], v[164:165], v[164:165]
	v_pk_mul_f32 v[236:237], v[150:151], v[150:151]
	v_add_f32_e32 v132, v232, v233
	v_add_f32_e32 v142, v228, v229
	v_pk_fma_f32 v[236:237], v[148:149], v[148:149], v[236:237]
	v_add_f32_e32 v132, v234, v132
	v_add_f32_e32 v142, v230, v142
	v_pk_fma_f32 v[236:237], v[156:157], v[156:157], v[236:237]
	v_pk_mul_f32 v[238:239], v[94:95], v[94:95]
	v_add_f32_e32 v132, v235, v132
	v_add_f32_e32 v142, v231, v142
	v_pk_fma_f32 v[236:237], v[158:159], v[158:159], v[236:237]
	v_pk_fma_f32 v[238:239], v[92:93], v[92:93], v[238:239]
	v_add_f32_e32 v132, v142, v132
	v_pk_fma_f32 v[238:239], v[130:131], v[130:131], v[238:239]
	v_pk_mul_f32 v[240:241], v[82:83], v[82:83]
	v_add_f32_e32 v132, v132, v236
	v_pk_fma_f32 v[238:239], v[134:135], v[134:135], v[238:239]
	v_pk_fma_f32 v[240:241], v[80:81], v[80:81], v[240:241]
	v_add_f32_e32 v132, v132, v237
	v_pk_fma_f32 v[240:241], v[84:85], v[84:85], v[240:241]
	v_add_f32_e32 v132, v132, v238
	v_pk_fma_f32 v[240:241], v[86:87], v[86:87], v[240:241]
	v_add_f32_e32 v132, v132, v239
	v_add_f32_e32 v132, v132, v240
	v_add_f32_e32 v132, v132, v241
	v_cvt_pk_f32_fp8_sdwa v[184:185], v155 src0_sel:WORD_1
	v_cvt_pk_f32_fp8_sdwa v[154:155], v154 src0_sel:WORD_1
	v_add_f32_dpp v132, v132, v132 quad_perm:[1,0,3,2] row_mask:0xf bank_mask:0xf bound_ctrl:1
	v_mov_b32_e32 v128, v91
	v_pk_add_f32 v[90:91], v[128:129], v[186:187]
	v_add_f32_dpp v132, v132, v132 quad_perm:[2,3,0,1] row_mask:0xf bank_mask:0xf bound_ctrl:1
	v_mov_b32_e32 v187, v154
	v_mov_b32_e32 v186, v184
	v_add_f32_dpp v132, v132, v132 row_half_mirror row_mask:0xf bank_mask:0xf bound_ctrl:1
	v_lshlrev_b64 v[234:235], 2, v[78:79]
	v_lshlrev_b32_e32 v129, 16, v143
	v_add_f32_dpp v132, v132, v132 row_mirror row_mask:0xf bank_mask:0xf bound_ctrl:1
	v_lshlrev_b32_e32 v128, 16, v133
	v_readlane_b32 s8, v132, 16
	v_readlane_b32 s9, v132, 48
	v_readlane_b32 s6, v132, 0
	v_readlane_b32 s7, v132, 32
	v_mov_b32_e32 v228, s8
	v_mov_b32_e32 v229, s9
	v_pk_add_f32 v[228:229], s[6:7], v[228:229]
	v_pk_add_f32 v[128:129], v[186:187], v[128:129]
	v_add_f32_e32 v132, v228, v229
	v_fmamk_f32 v132, v132, 0x3a000000, v206
	v_mul_f32_e32 v142, 0x4f800000, v132
	v_cmp_gt_f32_e32 vcc, s49, v132
	v_and_b32_e32 v143, 0xffff0000, v143
	v_pk_mul_f32 v[228:229], v[180:181], v[180:181]
	v_cndmask_b32_e32 v132, v132, v142, vcc
	v_sqrt_f32_e32 v142, v132
	v_pk_mul_f32 v[238:239], v[182:183], v[182:183]
	v_add_f32_e32 v228, v228, v229
	v_add_f32_e32 v228, v238, v228
	v_add_u32_e32 v154, -1, v142
	v_fma_f32 v160, -v154, v142, v132
	v_cmp_ge_f32_e64 s[6:7], 0, v160
	v_add_u32_e32 v160, 1, v142
	v_pk_mul_f32 v[242:243], v[138:139], v[138:139]
	v_cndmask_b32_e64 v154, v142, v154, s[6:7]
	v_fma_f32 v142, -v160, v142, v132
	v_cmp_lt_f32_e64 s[6:7], 0, v142
	v_add_f32_e32 v228, v239, v228
	v_pk_fma_f32 v[242:243], v[136:137], v[136:137], v[242:243]
	v_cndmask_b32_e64 v142, v154, v160, s[6:7]
	v_mul_f32_e32 v154, 0x37800000, v142
	v_cndmask_b32_e32 v142, v142, v154, vcc
	v_cmp_class_f32_e32 vcc, v132, v207
	v_mov_b32_e32 v154, v185
	v_pk_mul_f32 v[184:185], v[172:173], v[172:173]
	v_cndmask_b32_e32 v160, v142, v132, vcc
	v_div_scale_f32 v166, s[6:7], v160, v160, 1.0
	s_ashr_i32 s6, s18, 12
	s_add_i32 s6, s6, 4
	s_mul_hi_i32 s7, s6, 0xc000
	s_mul_i32 s6, s6, 0xc000
	s_add_u32 s6, s2, s6
	s_addc_u32 s7, s3, s7
	s_add_u32 s10, s6, 0xe000
	s_addc_u32 s11, s7, 0
	v_pk_fma_f32 v[230:231], v[168:169], v[168:169], v[184:185]
	s_add_u32 s12, s6, 0x10000
	s_addc_u32 s13, s7, 0
	v_pk_fma_f32 v[230:231], v[176:177], v[176:177], v[230:231]
	v_lshl_add_u64 v[184:185], s[12:13], 0, v[234:235]
	v_pk_fma_f32 v[240:241], v[178:179], v[178:179], v[230:231]
	v_lshl_add_u64 v[230:231], s[22:23], 0, v[234:235]
	v_lshlrev_b32_e32 v250, 4, v189
	v_add_u32_e32 v251, 0x1000, v250
	global_load_dwordx4 v[96:99], v250, s[12:13]
	global_load_dwordx4 v[100:103], v250, s[22:23]
	global_load_dwordx4 v[104:107], v250, s[10:11]
	global_load_dwordx4 v[108:111], v250, s[12:13] offset:1024
	global_load_dwordx4 v[112:115], v250, s[22:23] offset:1024
	global_load_dwordx4 v[116:119], v250, s[10:11] offset:1024
	global_load_dwordx4 v[120:123], v250, s[12:13] offset:2048
	global_load_dwordx4 v[124:127], v250, s[22:23] offset:2048
	global_load_dwordx4 v[212:215], v250, s[10:11] offset:2048
	global_load_dwordx4 v[216:219], v250, s[12:13] offset:3072
	global_load_dwordx4 v[220:223], v250, s[22:23] offset:3072
	global_load_dwordx4 v[224:227], v250, s[10:11] offset:3072
	v_lshl_add_u64 v[234:235], s[10:11], 0, v[234:235]
	v_rcp_f32_e32 v246, v166
	v_and_b32_e32 v142, 0xffff0000, v133
	v_pk_add_f32 v[132:133], v[154:155], v[142:143]
	v_fma_f32 v142, -v166, v246, 1.0
	v_fmac_f32_e32 v246, v142, v246
	v_pk_mul_f32 v[142:143], v[170:171], v[170:171]
	v_pk_mul_f32 v[154:155], v[174:175], v[174:175]
	v_add_f32_e32 v142, v142, v143
	v_add_f32_e32 v142, v154, v142
	v_add_f32_e32 v142, v155, v142
	v_add_f32_e32 v142, v142, v228
	v_pk_fma_f32 v[242:243], v[140:141], v[140:141], v[242:243]
	v_pk_mul_f32 v[244:245], v[90:91], v[90:91]
	v_add_f32_e32 v142, v142, v240
	v_pk_fma_f32 v[242:243], v[144:145], v[144:145], v[242:243]
	v_pk_fma_f32 v[244:245], v[88:89], v[88:89], v[244:245]
	v_add_f32_e32 v142, v142, v241
	v_pk_fma_f32 v[244:245], v[128:129], v[128:129], v[244:245]
	v_add_f32_e32 v142, v142, v242
	v_pk_fma_f32 v[244:245], v[132:133], v[132:133], v[244:245]
	v_add_f32_e32 v142, v142, v243
	v_add_f32_e32 v142, v142, v244
	v_add_f32_e32 v142, v142, v245
	v_div_scale_f32 v247, vcc, 1.0, v160, 1.0
	s_nop 0
	v_add_f32_dpp v142, v142, v142 quad_perm:[1,0,3,2] row_mask:0xf bank_mask:0xf bound_ctrl:1
	v_mul_f32_e32 v248, v247, v246
	v_fma_f32 v154, -v166, v248, v247
	v_add_f32_dpp v142, v142, v142 quad_perm:[2,3,0,1] row_mask:0xf bank_mask:0xf bound_ctrl:1
	v_fmac_f32_e32 v248, v154, v246
	v_fma_f32 v154, -v166, v248, v247
	v_add_f32_dpp v142, v142, v142 row_half_mirror row_mask:0xf bank_mask:0xf bound_ctrl:1
	v_div_fmas_f32 v154, v154, v246, v248
	v_lshrrev_b32_e32 v229, 1, v189
	v_add_f32_dpp v142, v142, v142 row_mirror row_mask:0xf bank_mask:0xf bound_ctrl:1
	v_add_u32_e32 v246, 64, v229
	v_readlane_b32 s8, v142, 16
	v_readlane_b32 s9, v142, 48
	v_readlane_b32 s6, v142, 0
	v_readlane_b32 s7, v142, 32
	v_mov_b32_e32 v142, s8
	v_mov_b32_e32 v143, s9
	v_pk_add_f32 v[142:143], s[6:7], v[142:143]
	s_ashr_i32 s19, s18, 31
	v_add_f32_e32 v142, v142, v143
	v_fmamk_f32 v142, v142, 0x3a000000, v206
	v_mul_f32_e32 v143, 0x4f800000, v142
	v_cmp_gt_f32_e64 s[6:7], s49, v142
	s_waitcnt vmcnt(11)
	v_pk_add_f32 v[96:97], v[96:97], 1.0 op_sel_hi:[1,0]
	v_cndmask_b32_e64 v142, v142, v143, s[6:7]
	v_sqrt_f32_e32 v143, v142
	s_nop 0
	v_add_u32_e32 v155, -1, v143
	v_fma_f32 v166, -v155, v143, v142
	v_cmp_ge_f32_e64 s[8:9], 0, v166
	v_add_u32_e32 v166, 1, v143
	s_nop 0
	v_cndmask_b32_e64 v155, v143, v155, s[8:9]
	v_fma_f32 v143, -v166, v143, v142
	v_cmp_lt_f32_e64 s[8:9], 0, v143
	s_nop 1
	v_cndmask_b32_e64 v143, v155, v166, s[8:9]
	v_mul_f32_e32 v155, 0x37800000, v143
	v_cndmask_b32_e64 v143, v143, v155, s[6:7]
	v_cmp_class_f32_e64 s[6:7], v142, v207
	v_div_fixup_f32 v166, v154, v160, 1.0
	v_pk_mul_f32 v[146:147], v[146:147], v[166:167] op_sel_hi:[1,0]
	v_cndmask_b32_e64 v142, v143, v142, s[6:7]
	v_div_scale_f32 v143, s[6:7], v142, v142, 1.0
	v_rcp_f32_e32 v155, v143
	s_waitcnt vmcnt(10)
	v_pk_mul_f32 v[146:147], v[100:101], v[146:147]
	v_pk_mul_f32 v[152:153], v[152:153], v[166:167] op_sel_hi:[1,0]
	v_pk_mul_f32 v[164:165], v[164:165], v[166:167] op_sel_hi:[1,0]
	v_fma_f32 v154, -v143, v155, 1.0
	v_fmac_f32_e32 v155, v154, v155
	v_div_scale_f32 v154, vcc, 1.0, v142, 1.0
	v_mul_f32_e32 v160, v154, v155
	v_fma_f32 v228, -v143, v160, v154
	v_fmac_f32_e32 v160, v228, v155
	v_fma_f32 v143, -v143, v160, v154
	v_div_fmas_f32 v143, v143, v155, v160
	v_div_fixup_f32 v160, v143, v142, 1.0
	v_lshlrev_b32_e32 v142, 3, v189
	v_and_b32_e32 v228, 8, v142
	v_pk_add_f32 v[142:143], v[98:99], 1.0 op_sel_hi:[1,0]
	s_waitcnt vmcnt(9)
	v_pk_fma_f32 v[154:155], v[96:97], v[146:147], v[104:105]
	v_pk_mul_f32 v[152:153], v[102:103], v[152:153]
	v_cvt_pk_bf16_f32 v146, v154, v155
	v_pk_mul_f32 v[170:171], v[170:171], v[160:161] op_sel_hi:[1,0]
	v_lshlrev_b32_e32 v186, 16, v146
	v_and_b32_e32 v187, 0xffff0000, v146
	v_sub_f32_e32 v186, v154, v186
	v_sub_f32_e32 v187, v155, v187
	v_pk_fma_f32 v[152:153], v[142:143], v[152:153], v[106:107]
	v_pk_mul_f32 v[170:171], v[100:101], v[170:171]
	v_cvt_pk_bf16_f32 v147, v152, v153
	v_cvt_pk_bf16_f32 v186, v186, v187
	v_pk_mul_f32 v[162:163], v[162:163], v[166:167] op_sel_hi:[1,0]
	v_lshlrev_b32_e32 v187, 16, v147
	v_and_b32_e32 v238, 0xffff0000, v147
	v_sub_f32_e32 v187, v152, v187
	v_sub_f32_e32 v238, v153, v238
	v_cvt_pk_bf16_f32 v187, v187, v238
	v_xor_b32_e32 v238, s43, v229
	v_lshlrev_b32_e32 v238, 4, v238
	v_add3_u32 v238, s44, v238, v228
	ds_write_b64 v238, v[146:147]
	v_add_u32_e32 v146, 0x10000, v238
	ds_write_b64 v146, v[186:187]
	v_pk_mul_f32 v[146:147], v[174:175], v[160:161] op_sel_hi:[1,0]
	v_xor_b32_e32 v238, s45, v229
	v_pk_mul_f32 v[146:147], v[102:103], v[146:147]
	v_lshlrev_b32_e32 v238, 4, v238
	v_pk_fma_f32 v[142:143], v[142:143], v[146:147], v[106:107]
	v_pk_fma_f32 v[146:147], v[96:97], v[170:171], v[104:105]
	v_lshlrev_b64 v[234:235], 2, v[76:77]
	v_cvt_pk_bf16_f32 v170, v146, v147
	v_cvt_pk_bf16_f32 v171, v142, v143
	v_lshl_add_u64 v[230:231], s[22:23], 0, v[234:235]
	v_lshlrev_b32_e32 v174, 16, v170
	v_and_b32_e32 v175, 0xffff0000, v170
	v_sub_f32_e32 v174, v146, v174
	v_sub_f32_e32 v175, v147, v175
	v_cvt_pk_bf16_f32 v174, v174, v175
	v_lshlrev_b32_e32 v175, 16, v171
	v_and_b32_e32 v184, 0xffff0000, v171
	v_sub_f32_e32 v175, v142, v175
	v_sub_f32_e32 v184, v143, v184
	v_cvt_pk_bf16_f32 v175, v175, v184
	v_lshl_add_u64 v[184:185], s[12:13], 0, v[234:235]
	global_load_dwordx4 v[96:99], v251, s[12:13]
	global_load_dwordx4 v[100:103], v251, s[22:23]
	global_load_dwordx4 v[104:107], v251, s[10:11]
	v_lshl_add_u64 v[234:235], s[10:11], 0, v[234:235]
	v_add3_u32 v238, s46, v238, v228
	ds_write_b64 v238, v[170:171]
	v_add_u32_e32 v170, 0x10000, v238
	ds_write_b64 v170, v[174:175]
	v_add_u32_e32 v238, 32, v229
	s_lshl_b64 s[6:7], s[18:19], 11
	s_add_u32 s6, s41, s6
	s_addc_u32 s7, s42, s7
	s_waitcnt vmcnt(11)
	v_pk_add_f32 v[110:111], v[110:111], 1.0 op_sel_hi:[1,0]
	v_pk_add_f32 v[108:109], v[108:109], 1.0 op_sel_hi:[1,0]
	s_waitcnt vmcnt(10)
	v_pk_mul_f32 v[162:163], v[162:163], v[112:113]
	v_pk_mul_f32 v[164:165], v[164:165], v[114:115]
	s_waitcnt vmcnt(9)
	v_pk_fma_f32 v[174:175], v[162:163], v[108:109], v[116:117]
	v_pk_fma_f32 v[170:171], v[164:165], v[110:111], v[118:119]
	v_cvt_pk_bf16_f32 v162, v174, v175
	s_nop 0
	v_lshlrev_b32_e32 v164, 16, v162
	v_and_b32_e32 v165, 0xffff0000, v162
	v_sub_f32_e32 v164, v174, v164
	v_sub_f32_e32 v165, v175, v165
	v_cvt_pk_bf16_f32 v163, v170, v171
	v_cvt_pk_bf16_f32 v164, v164, v165
	s_nop 0
	v_lshlrev_b32_e32 v165, 16, v163
	v_and_b32_e32 v239, 0xffff0000, v163
	v_sub_f32_e32 v165, v170, v165
	v_sub_f32_e32 v239, v171, v239
	v_cvt_pk_bf16_f32 v165, v165, v239
	v_xor_b32_e32 v239, s43, v238
	v_lshlrev_b32_e32 v239, 4, v239
	v_add3_u32 v239, s44, v239, v228
	ds_write_b64 v239, v[162:163]
	v_add_u32_e32 v162, 0x10000, v239
	ds_write_b64 v162, v[164:165]
	v_pk_mul_f32 v[164:165], v[180:181], v[160:161] op_sel_hi:[1,0]
	v_pk_mul_f32 v[162:163], v[182:183], v[160:161] op_sel_hi:[1,0]
	v_pk_mul_f32 v[164:165], v[164:165], v[112:113]
	v_pk_mul_f32 v[162:163], v[162:163], v[114:115]
	v_pk_fma_f32 v[164:165], v[164:165], v[108:109], v[116:117]
	v_pk_fma_f32 v[162:163], v[162:163], v[110:111], v[118:119]
	v_cvt_pk_bf16_f32 v184, v164, v165
	v_lshlrev_b64 v[234:235], 2, v[74:75]
	v_lshlrev_b32_e32 v180, 16, v184
	v_and_b32_e32 v181, 0xffff0000, v184
	v_sub_f32_e32 v180, v164, v180
	v_sub_f32_e32 v181, v165, v181
	v_cvt_pk_bf16_f32 v185, v162, v163
	v_cvt_pk_bf16_f32 v186, v180, v181
	v_lshl_add_u64 v[230:231], s[22:23], 0, v[234:235]
	v_lshlrev_b32_e32 v180, 16, v185
	v_and_b32_e32 v181, 0xffff0000, v185
	v_sub_f32_e32 v180, v162, v180
	v_sub_f32_e32 v181, v163, v181
	v_cvt_pk_bf16_f32 v187, v180, v181
	v_lshl_add_u64 v[180:181], s[12:13], 0, v[234:235]
	global_load_dwordx4 v[108:111], v251, s[12:13] offset:1024
	global_load_dwordx4 v[112:115], v251, s[22:23] offset:1024
	global_load_dwordx4 v[116:119], v251, s[10:11] offset:1024
	v_lshl_add_u64 v[234:235], s[10:11], 0, v[234:235]
	v_xor_b32_e32 v238, s45, v238
	v_lshlrev_b32_e32 v238, 4, v238
	v_add3_u32 v238, s46, v238, v228
	ds_write_b64 v238, v[184:185]
	v_add_u32_e32 v184, 0x10000, v238
	ds_write_b64 v184, v[186:187]
	v_mov_b32_e32 v184, v148
	v_mov_b32_e32 v185, v150
	v_pk_mul_f32 v[184:185], v[184:185], v[166:167] op_sel_hi:[1,0]
	s_waitcnt vmcnt(11)
	v_pk_add_f32 v[238:239], v[120:121], 1.0 op_sel_hi:[1,0]
	v_mov_b32_e32 v180, v156
	v_mov_b32_e32 v181, v158
	v_pk_mul_f32 v[180:181], v[180:181], v[166:167] op_sel_hi:[1,0]
	v_pk_add_f32 v[122:123], v[122:123], 1.0 op_sel_hi:[1,0]
	s_waitcnt vmcnt(10)
	v_pk_mul_f32 v[186:187], v[184:185], v[124:125]
	v_pk_mul_f32 v[180:181], v[180:181], v[126:127]
	s_waitcnt vmcnt(9)
	v_pk_fma_f32 v[186:187], v[186:187], v[238:239], v[212:213]
	v_pk_fma_f32 v[184:185], v[180:181], v[122:123], v[214:215]
	v_cvt_pk_bf16_f32 v180, v186, v187
	v_mov_b32_e32 v158, v157
	v_lshlrev_b32_e32 v148, 16, v180
	v_sub_f32_e32 v148, v186, v148
	v_and_b32_e32 v150, 0xffff0000, v180
	v_cvt_pk_bf16_f32 v181, v184, v185
	v_sub_f32_e32 v150, v187, v150
	v_cvt_pk_bf16_f32 v240, v148, v150
	v_lshlrev_b32_e32 v148, 16, v181
	v_sub_f32_e32 v148, v184, v148
	v_and_b32_e32 v150, 0xffff0000, v181
	v_sub_f32_e32 v150, v185, v150
	v_cvt_pk_bf16_f32 v241, v148, v150
	v_xor_b32_e32 v148, s43, v246
	v_lshlrev_b32_e32 v148, 4, v148
	v_add3_u32 v148, s44, v148, v228
	ds_write_b64 v148, v[180:181]
	v_add_u32_e32 v148, 0x10000, v148
	ds_write_b64 v148, v[240:241]
	v_mov_b32_e32 v180, v176
	v_mov_b32_e32 v181, v178
	v_mov_b32_e32 v240, v168
	v_mov_b32_e32 v241, v172
	v_pk_mul_f32 v[180:181], v[180:181], v[160:161] op_sel_hi:[1,0]
	v_pk_mul_f32 v[240:241], v[240:241], v[160:161] op_sel_hi:[1,0]
	v_pk_mul_f32 v[180:181], v[180:181], v[126:127]
	v_pk_mul_f32 v[124:125], v[240:241], v[124:125]
	v_pk_fma_f32 v[180:181], v[180:181], v[122:123], v[214:215]
	v_pk_fma_f32 v[182:183], v[124:125], v[238:239], v[212:213]
	v_lshlrev_b64 v[238:239], 2, v[72:73]
	v_cvt_pk_bf16_f32 v242, v182, v183
	v_cvt_pk_bf16_f32 v243, v180, v181
	v_lshl_add_u64 v[230:231], s[12:13], 0, v[238:239]
	v_lshlrev_b32_e32 v148, 16, v242
	v_and_b32_e32 v150, 0xffff0000, v242
	v_sub_f32_e32 v148, v182, v148
	v_sub_f32_e32 v150, v183, v150
	v_cvt_pk_bf16_f32 v244, v148, v150
	v_lshlrev_b32_e32 v148, 16, v243
	v_and_b32_e32 v150, 0xffff0000, v243
	v_lshl_add_u64 v[234:235], s[22:23], 0, v[238:239]
	v_sub_f32_e32 v148, v180, v148
	v_sub_f32_e32 v150, v181, v150
	v_cvt_pk_bf16_f32 v245, v148, v150
	global_load_dwordx4 v[120:123], v251, s[12:13] offset:2048
	global_load_dwordx4 v[124:127], v251, s[22:23] offset:2048
	global_load_dwordx4 v[212:215], v251, s[10:11] offset:2048
	v_lshl_add_u64 v[238:239], s[10:11], 0, v[238:239]
	v_xor_b32_e32 v148, s45, v246
	v_lshlrev_b32_e32 v148, 4, v148
	v_add3_u32 v148, s46, v148, v228
	ds_write_b64 v148, v[242:243]
	v_add_u32_e32 v148, 0x10000, v148
	v_mov_b32_e32 v150, v149
	ds_write_b64 v148, v[244:245]
	v_pk_mul_f32 v[156:157], v[158:159], v[166:167] op_sel_hi:[1,0]
	v_pk_mul_f32 v[148:149], v[150:151], v[166:167] op_sel_hi:[1,0]
	v_add_u32_e32 v242, 0x60, v229
	v_mov_b32_e32 v172, v169
	v_mov_b32_e32 v178, v177
	v_add_u32_e32 v246, 0x80, v229
	s_waitcnt vmcnt(11)
	v_pk_add_f32 v[218:219], v[218:219], 1.0 op_sel_hi:[1,0]
	v_pk_add_f32 v[216:217], v[216:217], 1.0 op_sel_hi:[1,0]
	s_waitcnt vmcnt(10)
	v_pk_mul_f32 v[148:149], v[148:149], v[220:221]
	v_pk_mul_f32 v[150:151], v[156:157], v[222:223]
	s_waitcnt vmcnt(9)
	v_pk_fma_f32 v[158:159], v[148:149], v[216:217], v[224:225]
	v_pk_fma_f32 v[156:157], v[150:151], v[218:219], v[226:227]
	v_cvt_pk_bf16_f32 v148, v158, v159
	s_nop 0
	v_lshlrev_b32_e32 v150, 16, v148
	v_and_b32_e32 v151, 0xffff0000, v148
	v_sub_f32_e32 v150, v158, v150
	v_sub_f32_e32 v151, v159, v151
	v_cvt_pk_bf16_f32 v149, v156, v157
	v_cvt_pk_bf16_f32 v150, v150, v151
	s_nop 0
	v_lshlrev_b32_e32 v151, 16, v149
	v_and_b32_e32 v168, 0xffff0000, v149
	v_sub_f32_e32 v151, v156, v151
	v_sub_f32_e32 v168, v157, v168
	v_cvt_pk_bf16_f32 v151, v151, v168
	v_xor_b32_e32 v168, s43, v242
	v_lshlrev_b32_e32 v168, 4, v168
	v_add3_u32 v168, s44, v168, v228
	ds_write_b64 v168, v[148:149]
	v_add_u32_e32 v148, 0x10000, v168
	ds_write_b64 v148, v[150:151]
	v_pk_mul_f32 v[150:151], v[172:173], v[160:161] op_sel_hi:[1,0]
	v_pk_mul_f32 v[148:149], v[178:179], v[160:161] op_sel_hi:[1,0]
	v_pk_mul_f32 v[150:151], v[150:151], v[220:221]
	v_pk_mul_f32 v[148:149], v[148:149], v[222:223]
	v_pk_fma_f32 v[150:151], v[150:151], v[216:217], v[224:225]
	v_pk_fma_f32 v[148:149], v[148:149], v[218:219], v[226:227]
	v_cvt_pk_bf16_f32 v168, v150, v151
	v_lshlrev_b64 v[234:235], 2, v[70:71]
	v_lshlrev_b32_e32 v172, 16, v168
	v_and_b32_e32 v173, 0xffff0000, v168
	v_sub_f32_e32 v172, v150, v172
	v_sub_f32_e32 v173, v151, v173
	v_cvt_pk_bf16_f32 v169, v148, v149
	v_cvt_pk_bf16_f32 v172, v172, v173
	v_lshl_add_u64 v[230:231], s[22:23], 0, v[234:235]
	v_lshlrev_b32_e32 v173, 16, v169
	v_and_b32_e32 v176, 0xffff0000, v169
	v_sub_f32_e32 v173, v148, v173
	v_sub_f32_e32 v176, v149, v176
	v_cvt_pk_bf16_f32 v173, v173, v176
	v_lshl_add_u64 v[176:177], s[12:13], 0, v[234:235]
	global_load_dwordx4 v[216:219], v251, s[12:13] offset:3072
	global_load_dwordx4 v[220:223], v251, s[22:23] offset:3072
	global_load_dwordx4 v[224:227], v251, s[10:11] offset:3072
	v_lshl_add_u64 v[234:235], s[10:11], 0, v[234:235]
	v_xor_b32_e32 v238, s45, v242
	v_lshlrev_b32_e32 v238, 4, v238
	v_add3_u32 v238, s46, v238, v228
	ds_write_b64 v238, v[168:169]
	v_add_u32_e32 v168, 0x10000, v238
	ds_write_b64 v168, v[172:173]
	s_waitcnt vmcnt(11)
	v_pk_add_f32 v[168:169], v[98:99], 1.0 op_sel_hi:[1,0]
	v_mov_b32_e32 v178, v92
	v_mov_b32_e32 v179, v94
	v_pk_mul_f32 v[178:179], v[178:179], v[166:167] op_sel_hi:[1,0]
	v_pk_add_f32 v[172:173], v[96:97], 1.0 op_sel_hi:[1,0]
	v_mov_b32_e32 v176, v130
	v_mov_b32_e32 v177, v134
	s_waitcnt vmcnt(10)
	v_pk_mul_f32 v[178:179], v[178:179], v[100:101]
	v_pk_mul_f32 v[176:177], v[176:177], v[166:167] op_sel_hi:[1,0]
	s_waitcnt vmcnt(9)
	v_pk_fma_f32 v[178:179], v[178:179], v[172:173], v[104:105]
	v_pk_mul_f32 v[176:177], v[176:177], v[102:103]
	v_cvt_pk_bf16_f32 v238, v178, v179
	v_mov_b32_e32 v134, v131
	v_lshlrev_b32_e32 v92, 16, v238
	v_sub_f32_e32 v92, v178, v92
	v_and_b32_e32 v94, 0xffff0000, v238
	v_pk_fma_f32 v[176:177], v[176:177], v[168:169], v[106:107]
	v_sub_f32_e32 v94, v179, v94
	v_cvt_pk_bf16_f32 v239, v176, v177
	v_cvt_pk_bf16_f32 v240, v92, v94
	v_pk_mul_f32 v[130:131], v[134:135], v[166:167] op_sel_hi:[1,0]
	v_lshlrev_b32_e32 v92, 16, v239
	v_sub_f32_e32 v92, v176, v92
	v_and_b32_e32 v94, 0xffff0000, v239
	v_sub_f32_e32 v94, v177, v94
	v_cvt_pk_bf16_f32 v241, v92, v94
	v_xor_b32_e32 v92, s43, v246
	v_lshlrev_b32_e32 v92, 4, v92
	v_add3_u32 v92, s44, v92, v228
	ds_write_b64 v92, v[238:239]
	v_add_u32_e32 v92, 0x10000, v92
	ds_write_b64 v92, v[240:241]
	v_mov_b32_e32 v240, v136
	v_mov_b32_e32 v241, v138
	v_pk_mul_f32 v[240:241], v[240:241], v[160:161] op_sel_hi:[1,0]
	v_mov_b32_e32 v238, v140
	v_mov_b32_e32 v239, v144
	v_pk_mul_f32 v[100:101], v[240:241], v[100:101]
	v_pk_mul_f32 v[238:239], v[238:239], v[160:161] op_sel_hi:[1,0]
	v_pk_fma_f32 v[172:173], v[100:101], v[172:173], v[104:105]
	v_pk_mul_f32 v[102:103], v[238:239], v[102:103]
	v_cvt_pk_bf16_f32 v242, v172, v173
	v_lshlrev_b64 v[238:239], 2, v[68:69]
	v_lshlrev_b32_e32 v92, 16, v242
	v_and_b32_e32 v94, 0xffff0000, v242
	v_sub_f32_e32 v92, v172, v92
	v_sub_f32_e32 v94, v173, v94
	v_pk_fma_f32 v[168:169], v[102:103], v[168:169], v[106:107]
	v_lshl_add_u64 v[230:231], s[12:13], 0, v[238:239]
	v_cvt_pk_bf16_f32 v243, v168, v169
	v_cvt_pk_bf16_f32 v244, v92, v94
	v_lshl_add_u64 v[234:235], s[22:23], 0, v[238:239]
	v_lshlrev_b32_e32 v92, 16, v243
	v_and_b32_e32 v94, 0xffff0000, v243
	v_sub_f32_e32 v92, v168, v92
	v_sub_f32_e32 v94, v169, v94
	v_cvt_pk_bf16_f32 v245, v92, v94
	v_lshl_add_u64 v[238:239], s[10:11], 0, v[238:239]
	v_xor_b32_e32 v92, s45, v246
	v_lshlrev_b32_e32 v92, 4, v92
	v_add3_u32 v92, s46, v92, v228
	ds_write_b64 v92, v[242:243]
	v_add_u32_e32 v92, 0x10000, v92
	v_mov_b32_e32 v94, v93
	ds_write_b64 v92, v[244:245]
	v_pk_mul_f32 v[92:93], v[94:95], v[166:167] op_sel_hi:[1,0]
	v_add_u32_e32 v242, 0xa0, v229
	v_mov_b32_e32 v138, v137
	v_mov_b32_e32 v144, v141
	v_add_u32_e32 v246, 0xc0, v229
	s_waitcnt vmcnt(8)
	v_pk_add_f32 v[110:111], v[110:111], 1.0 op_sel_hi:[1,0]
	v_pk_add_f32 v[108:109], v[108:109], 1.0 op_sel_hi:[1,0]
	s_waitcnt vmcnt(7)
	v_pk_mul_f32 v[92:93], v[92:93], v[112:113]
	v_pk_mul_f32 v[94:95], v[130:131], v[114:115]
	s_waitcnt vmcnt(6)
	v_pk_fma_f32 v[134:135], v[92:93], v[108:109], v[116:117]
	v_pk_fma_f32 v[130:131], v[94:95], v[110:111], v[118:119]
	v_cvt_pk_bf16_f32 v92, v134, v135
	s_nop 0
	v_lshlrev_b32_e32 v94, 16, v92
	v_and_b32_e32 v95, 0xffff0000, v92
	v_sub_f32_e32 v94, v134, v94
	v_sub_f32_e32 v95, v135, v95
	v_cvt_pk_bf16_f32 v93, v130, v131
	v_cvt_pk_bf16_f32 v94, v94, v95
	s_nop 0
	v_lshlrev_b32_e32 v95, 16, v93
	v_and_b32_e32 v136, 0xffff0000, v93
	v_sub_f32_e32 v95, v130, v95
	v_sub_f32_e32 v136, v131, v136
	v_cvt_pk_bf16_f32 v95, v95, v136
	v_xor_b32_e32 v136, s43, v242
	v_lshlrev_b32_e32 v136, 4, v136
	v_add3_u32 v136, s44, v136, v228
	ds_write_b64 v136, v[92:93]
	v_add_u32_e32 v92, 0x10000, v136
	ds_write_b64 v92, v[94:95]
	v_pk_mul_f32 v[94:95], v[138:139], v[160:161] op_sel_hi:[1,0]
	v_pk_mul_f32 v[92:93], v[144:145], v[160:161] op_sel_hi:[1,0]
	v_pk_mul_f32 v[94:95], v[94:95], v[112:113]
	v_pk_mul_f32 v[92:93], v[92:93], v[114:115]
	v_pk_fma_f32 v[94:95], v[94:95], v[108:109], v[116:117]
	v_pk_fma_f32 v[92:93], v[92:93], v[110:111], v[118:119]
	v_cvt_pk_bf16_f32 v140, v94, v95
	v_lshlrev_b64 v[234:235], 2, v[66:67]
	v_lshlrev_b32_e32 v136, 16, v140
	v_and_b32_e32 v137, 0xffff0000, v140
	v_sub_f32_e32 v136, v94, v136
	v_sub_f32_e32 v137, v95, v137
	v_cvt_pk_bf16_f32 v141, v92, v93
	v_cvt_pk_bf16_f32 v144, v136, v137
	v_lshl_add_u64 v[230:231], s[22:23], 0, v[234:235]
	v_lshlrev_b32_e32 v136, 16, v141
	v_and_b32_e32 v137, 0xffff0000, v141
	v_sub_f32_e32 v136, v92, v136
	v_sub_f32_e32 v137, v93, v137
	v_cvt_pk_bf16_f32 v145, v136, v137
	v_lshl_add_u64 v[136:137], s[12:13], 0, v[234:235]
	v_lshl_add_u64 v[234:235], s[10:11], 0, v[234:235]
	v_xor_b32_e32 v238, s45, v242
	v_lshlrev_b32_e32 v238, 4, v238
	v_add3_u32 v238, s46, v238, v228
	ds_write_b64 v238, v[140:141]
	v_add_u32_e32 v140, 0x10000, v238
	ds_write_b64 v140, v[144:145]
	v_mov_b32_e32 v144, v80
	v_mov_b32_e32 v145, v82
	v_pk_mul_f32 v[144:145], v[144:145], v[166:167] op_sel_hi:[1,0]
	s_waitcnt vmcnt(5)
	v_pk_add_f32 v[140:141], v[120:121], 1.0 op_sel_hi:[1,0]
	v_mov_b32_e32 v136, v84
	v_mov_b32_e32 v137, v86
	v_pk_mul_f32 v[136:137], v[136:137], v[166:167] op_sel_hi:[1,0]
	v_pk_add_f32 v[122:123], v[122:123], 1.0 op_sel_hi:[1,0]
	s_waitcnt vmcnt(4)
	v_pk_mul_f32 v[144:145], v[144:145], v[124:125]
	v_pk_mul_f32 v[136:137], v[136:137], v[126:127]
	s_waitcnt vmcnt(3)
	v_pk_fma_f32 v[144:145], v[144:145], v[140:141], v[212:213]
	v_pk_fma_f32 v[242:243], v[136:137], v[122:123], v[214:215]
	v_cvt_pk_bf16_f32 v136, v144, v145
	v_mov_b32_e32 v86, v85
	v_lshlrev_b32_e32 v80, 16, v136
	v_sub_f32_e32 v80, v144, v80
	v_and_b32_e32 v82, 0xffff0000, v136
	v_cvt_pk_bf16_f32 v137, v242, v243
	v_sub_f32_e32 v82, v145, v82
	v_cvt_pk_bf16_f32 v238, v80, v82
	v_lshlrev_b32_e32 v80, 16, v137
	v_sub_f32_e32 v80, v242, v80
	v_and_b32_e32 v82, 0xffff0000, v137
	v_sub_f32_e32 v82, v243, v82
	v_cvt_pk_bf16_f32 v239, v80, v82
	v_xor_b32_e32 v80, s43, v246
	v_lshlrev_b32_e32 v80, 4, v80
	v_add3_u32 v80, s44, v80, v228
	ds_write_b64 v80, v[136:137]
	v_add_u32_e32 v80, 0x10000, v80
	ds_write_b64 v80, v[238:239]
	v_mov_b32_e32 v136, v128
	v_mov_b32_e32 v137, v132
	v_mov_b32_e32 v238, v88
	v_mov_b32_e32 v239, v90
	v_pk_mul_f32 v[136:137], v[136:137], v[160:161] op_sel_hi:[1,0]
	v_pk_mul_f32 v[238:239], v[238:239], v[160:161] op_sel_hi:[1,0]
	v_pk_mul_f32 v[136:137], v[136:137], v[126:127]
	v_pk_mul_f32 v[124:125], v[238:239], v[124:125]
	v_pk_fma_f32 v[136:137], v[136:137], v[122:123], v[214:215]
	v_pk_fma_f32 v[138:139], v[124:125], v[140:141], v[212:213]
	v_lshlrev_b64 v[238:239], 2, v[64:65]
	v_cvt_pk_bf16_f32 v140, v138, v139
	v_cvt_pk_bf16_f32 v141, v136, v137
	v_lshl_add_u64 v[230:231], s[12:13], 0, v[238:239]
	v_lshlrev_b32_e32 v80, 16, v140
	v_and_b32_e32 v82, 0xffff0000, v140
	v_sub_f32_e32 v80, v138, v80
	v_sub_f32_e32 v82, v139, v82
	v_cvt_pk_bf16_f32 v244, v80, v82
	v_lshlrev_b32_e32 v80, 16, v141
	v_and_b32_e32 v82, 0xffff0000, v141
	v_lshl_add_u64 v[234:235], s[22:23], 0, v[238:239]
	v_sub_f32_e32 v80, v136, v80
	v_sub_f32_e32 v82, v137, v82
	v_cvt_pk_bf16_f32 v245, v80, v82
	v_lshl_add_u64 v[238:239], s[10:11], 0, v[238:239]
	v_xor_b32_e32 v80, s45, v246
	v_lshlrev_b32_e32 v80, 4, v80
	v_add3_u32 v80, s46, v80, v228
	ds_write_b64 v80, v[140:141]
	v_add_u32_e32 v80, 0x10000, v80
	v_mov_b32_e32 v82, v81
	ds_write_b64 v80, v[244:245]
	v_pk_mul_f32 v[80:81], v[82:83], v[166:167] op_sel_hi:[1,0]
	v_pk_mul_f32 v[84:85], v[86:87], v[166:167] op_sel_hi:[1,0]
	v_add_u32_e32 v128, 0xe0, v229
	v_mov_b32_e32 v90, v89
	v_mov_b32_e32 v132, v129
	s_waitcnt vmcnt(2)
	v_pk_add_f32 v[216:217], v[216:217], 1.0 op_sel_hi:[1,0]
	v_pk_add_f32 v[140:141], v[218:219], 1.0 op_sel_hi:[1,0]
	s_waitcnt vmcnt(1)
	v_pk_mul_f32 v[80:81], v[80:81], v[220:221]
	v_pk_mul_f32 v[82:83], v[84:85], v[222:223]
	s_waitcnt vmcnt(0)
	v_pk_fma_f32 v[80:81], v[80:81], v[216:217], v[224:225]
	v_pk_fma_f32 v[82:83], v[82:83], v[140:141], v[226:227]
	v_cvt_pk_bf16_f32 v84, v80, v81
	s_nop 0
	v_lshlrev_b32_e32 v86, 16, v84
	v_and_b32_e32 v87, 0xffff0000, v84
	v_sub_f32_e32 v86, v80, v86
	v_sub_f32_e32 v87, v81, v87
	v_cvt_pk_bf16_f32 v85, v82, v83
	v_cvt_pk_bf16_f32 v86, v86, v87
	s_nop 0
	v_lshlrev_b32_e32 v87, 16, v85
	v_and_b32_e32 v88, 0xffff0000, v85
	v_sub_f32_e32 v87, v82, v87
	v_sub_f32_e32 v88, v83, v88
	v_cvt_pk_bf16_f32 v87, v87, v88
	v_xor_b32_e32 v88, s43, v128
	v_lshlrev_b32_e32 v88, 4, v88
	v_add3_u32 v88, s44, v88, v228
	ds_write_b64 v88, v[84:85]
	v_add_u32_e32 v84, 0x10000, v88
	ds_write_b64 v84, v[86:87]
	v_pk_mul_f32 v[86:87], v[90:91], v[160:161] op_sel_hi:[1,0]
	v_pk_mul_f32 v[84:85], v[132:133], v[160:161] op_sel_hi:[1,0]
	v_pk_mul_f32 v[86:87], v[86:87], v[220:221]
	v_pk_mul_f32 v[84:85], v[84:85], v[222:223]
	v_pk_fma_f32 v[86:87], v[86:87], v[216:217], v[224:225]
	v_xor_b32_e32 v128, s45, v128
	v_cvt_pk_bf16_f32 v88, v86, v87
	v_pk_fma_f32 v[84:85], v[84:85], v[140:141], v[226:227]
	s_cmp_lt_i32 s56, s39
	s_cbranch_scc0 .Lpf_skip_1
	s_add_i32 s98, s38, s18
	s_ashr_i32 s99, s98, 31
	s_lshl_b64 s[100:101], s[98:99], 11
	s_lshl_b64 s[98:99], s[98:99], 12
	s_add_u32 s98, s35, s98
	s_addc_u32 s99, s36, s99
	s_add_u32 s100, s37, s100
	v_lshlrev_b64 v[112:113], 1, v[78:79]
	s_addc_u32 s101, s40, s101
	v_lshl_add_u64 v[110:111], s[98:99], 0, v[112:113]
	s_add_i32 s98, s47, s18
	s_ashr_i32 s99, s98, 31
	v_lshl_add_u64 v[114:115], s[100:101], 0, v[78:79]
	s_lshl_b64 s[100:101], s[98:99], 11
	s_lshl_b64 s[98:99], s[98:99], 12
	s_add_u32 s98, s35, s98
	s_addc_u32 s99, s36, s99
	s_add_u32 s100, s37, s100
	s_addc_u32 s101, s40, s101
	v_lshl_add_u64 v[126:127], s[98:99], 0, v[112:113]
	global_load_dwordx2 v[96:97], v[110:111], off
	global_load_dwordx2 v[98:99], v[110:111], off offset:512
	global_load_dwordx2 v[100:101], v[110:111], off offset:1024
	global_load_dwordx2 v[102:103], v[110:111], off offset:1536
	global_load_dwordx2 v[104:105], v[110:111], off offset:2048
	global_load_dwordx2 v[106:107], v[110:111], off offset:2560
	global_load_dwordx2 v[108:109], v[110:111], off offset:3072
	s_nop 0
	global_load_dwordx2 v[110:111], v[110:111], off offset:3584
	s_nop 0
	global_load_dword v212, v[114:115], off
	global_load_dword v213, v[114:115], off offset:256
	global_load_dword v214, v[114:115], off offset:512
	global_load_dword v215, v[114:115], off offset:768
	global_load_dword v216, v[114:115], off offset:1024
	global_load_dword v217, v[114:115], off offset:1280
	global_load_dword v218, v[114:115], off offset:1536
	global_load_dword v219, v[114:115], off offset:1792
	v_lshl_add_u64 v[250:251], s[100:101], 0, v[78:79]
	global_load_dwordx2 v[112:113], v[126:127], off
	global_load_dwordx2 v[114:115], v[126:127], off offset:512
	global_load_dwordx2 v[116:117], v[126:127], off offset:1024
	global_load_dwordx2 v[118:119], v[126:127], off offset:1536
	global_load_dwordx2 v[120:121], v[126:127], off offset:2048
	global_load_dwordx2 v[122:123], v[126:127], off offset:2560
	global_load_dwordx2 v[124:125], v[126:127], off offset:3072
	s_nop 0
	global_load_dwordx2 v[126:127], v[126:127], off offset:3584
	s_nop 0
	global_load_dword v220, v[250:251], off
	global_load_dword v221, v[250:251], off offset:256
	global_load_dword v222, v[250:251], off offset:512
	global_load_dword v223, v[250:251], off offset:768
	global_load_dword v224, v[250:251], off offset:1024
	global_load_dword v225, v[250:251], off offset:1280
	global_load_dword v226, v[250:251], off offset:1536
	global_load_dword v227, v[250:251], off offset:1792
